# MLP1: half of each non-final unit GELU epilogue (bj=1 groups) deferred into next K-loop at ~1.15 plain VALU per MFMA gap
# baseline (speedup 1.0000x reference)
.LBB5_42:
	s_and_b64 vcc, exec, s[0:1]
	s_cbranch_vccnz .Lg_orig_epi
	s_mul_i32 s40, s74, 0xc00
	s_add_i32 s40, s40, 0
	v_lshl_add_u32 v135, s73, 7, v111
	s_add_i32 s44, s40, 0x24000
	s_waitcnt lgkmcnt(0)
	v_mad_i64_i32 v[96:97], s[42:43], v135, s63, 0
	v_lshl_add_u64 v[126:127], v[96:97], 1, s[8:9]
	v_add_u32_e32 v96, s44, v129
	v_lshl_add_u32 v32, v110, 2, s44
	v_add_u32_e32 v136, 0x800, v96
	ds_read_b128 v[68:71], v32
	ds_read_b128 v[60:63], v32 offset:16
	ds_read_b128 v[64:67], v32 offset:1024
	ds_read_b128 v[56:59], v32 offset:1040
	ds_read_b128 v[44:47], v32 offset:512
	ds_read_b128 v[36:39], v32 offset:528
	ds_read_b128 v[40:43], v32 offset:1536
	ds_read_b128 v[32:35], v32 offset:1552
	ds_read2_b64 v[96:99], v136 offset1:16
	ds_read2_b64 v[240:243], v136 offset0:32 offset1:48
	s_lshl_b32 s40, s72, 8
	s_ashr_i32 s41, s40, 31
	s_lshl_b64 s[40:41], s[40:41], 1
	v_lshl_add_u64 v[126:127], v[126:127], 0, s[40:41]
	v_lshlrev_b32_e32 v108, 1, v110
	v_lshl_add_u64 v[250:251], v[126:127], 0, v[108:109]
	s_waitcnt lgkmcnt(0)
	v_pk_fma_f32 v[176:177], v[68:69], v[96:97], v[92:93] op_sel_hi:[1,0,1] neg_lo:[1,0,0] neg_hi:[1,0,0]
	v_pk_fma_f32 v[178:179], v[70:71], v[96:97], v[94:95] op_sel_hi:[1,0,1] neg_lo:[1,0,0] neg_hi:[1,0,0]
	v_pk_fma_f32 v[180:181], v[60:61], v[96:97], v[88:89] op_sel_hi:[1,0,1] neg_lo:[1,0,0] neg_hi:[1,0,0]
	v_pk_fma_f32 v[182:183], v[62:63], v[96:97], v[90:91] op_sel_hi:[1,0,1] neg_lo:[1,0,0] neg_hi:[1,0,0]
	v_pk_fma_f32 v[176:177], v[96:97], v[176:177], v[64:65] op_sel:[1,0,0]
	v_pk_fma_f32 v[178:179], v[96:97], v[178:179], v[66:67] op_sel:[1,0,0]
	v_pk_fma_f32 v[180:181], v[96:97], v[180:181], v[56:57] op_sel:[1,0,0]
	v_pk_fma_f32 v[182:183], v[96:97], v[182:183], v[58:59] op_sel:[1,0,0]
	v_pk_fma_f32 v[184:185], v[44:45], v[96:97], v[84:85] op_sel_hi:[1,0,1] neg_lo:[1,0,0] neg_hi:[1,0,0]
	v_pk_fma_f32 v[186:187], v[46:47], v[96:97], v[86:87] op_sel_hi:[1,0,1] neg_lo:[1,0,0] neg_hi:[1,0,0]
	v_pk_fma_f32 v[188:189], v[36:37], v[96:97], v[80:81] op_sel_hi:[1,0,1] neg_lo:[1,0,0] neg_hi:[1,0,0]
	v_pk_fma_f32 v[190:191], v[38:39], v[96:97], v[82:83] op_sel_hi:[1,0,1] neg_lo:[1,0,0] neg_hi:[1,0,0]
	v_pk_fma_f32 v[184:185], v[96:97], v[184:185], v[40:41] op_sel:[1,0,0]
	v_pk_fma_f32 v[186:187], v[96:97], v[186:187], v[42:43] op_sel:[1,0,0]
	v_pk_fma_f32 v[188:189], v[96:97], v[188:189], v[32:33] op_sel:[1,0,0]
	v_pk_fma_f32 v[190:191], v[96:97], v[190:191], v[34:35] op_sel:[1,0,0]
	v_pk_fma_f32 v[192:193], v[68:69], v[98:99], v[76:77] op_sel_hi:[1,0,1] neg_lo:[1,0,0] neg_hi:[1,0,0]
	v_pk_fma_f32 v[194:195], v[70:71], v[98:99], v[78:79] op_sel_hi:[1,0,1] neg_lo:[1,0,0] neg_hi:[1,0,0]
	v_pk_fma_f32 v[196:197], v[60:61], v[98:99], v[72:73] op_sel_hi:[1,0,1] neg_lo:[1,0,0] neg_hi:[1,0,0]
	v_pk_fma_f32 v[198:199], v[62:63], v[98:99], v[74:75] op_sel_hi:[1,0,1] neg_lo:[1,0,0] neg_hi:[1,0,0]
	v_pk_fma_f32 v[192:193], v[98:99], v[192:193], v[64:65] op_sel:[1,0,0]
	v_pk_fma_f32 v[194:195], v[98:99], v[194:195], v[66:67] op_sel:[1,0,0]
	v_pk_fma_f32 v[196:197], v[98:99], v[196:197], v[56:57] op_sel:[1,0,0]
	v_pk_fma_f32 v[198:199], v[98:99], v[198:199], v[58:59] op_sel:[1,0,0]
	v_pk_fma_f32 v[200:201], v[44:45], v[98:99], v[52:53] op_sel_hi:[1,0,1] neg_lo:[1,0,0] neg_hi:[1,0,0]
	v_pk_fma_f32 v[202:203], v[46:47], v[98:99], v[54:55] op_sel_hi:[1,0,1] neg_lo:[1,0,0] neg_hi:[1,0,0]
	v_pk_fma_f32 v[204:205], v[36:37], v[98:99], v[48:49] op_sel_hi:[1,0,1] neg_lo:[1,0,0] neg_hi:[1,0,0]
	v_pk_fma_f32 v[206:207], v[38:39], v[98:99], v[50:51] op_sel_hi:[1,0,1] neg_lo:[1,0,0] neg_hi:[1,0,0]
	v_pk_fma_f32 v[200:201], v[98:99], v[200:201], v[40:41] op_sel:[1,0,0]
	v_pk_fma_f32 v[202:203], v[98:99], v[202:203], v[42:43] op_sel:[1,0,0]
	v_pk_fma_f32 v[204:205], v[98:99], v[204:205], v[32:33] op_sel:[1,0,0]
	v_pk_fma_f32 v[206:207], v[98:99], v[206:207], v[34:35] op_sel:[1,0,0]
	v_pk_fma_f32 v[208:209], v[68:69], v[240:241], v[28:29] op_sel_hi:[1,0,1] neg_lo:[1,0,0] neg_hi:[1,0,0]
	v_pk_fma_f32 v[210:211], v[70:71], v[240:241], v[30:31] op_sel_hi:[1,0,1] neg_lo:[1,0,0] neg_hi:[1,0,0]
	v_pk_fma_f32 v[212:213], v[60:61], v[240:241], v[24:25] op_sel_hi:[1,0,1] neg_lo:[1,0,0] neg_hi:[1,0,0]
	v_pk_fma_f32 v[214:215], v[62:63], v[240:241], v[26:27] op_sel_hi:[1,0,1] neg_lo:[1,0,0] neg_hi:[1,0,0]
	v_pk_fma_f32 v[208:209], v[240:241], v[208:209], v[64:65] op_sel:[1,0,0]
	v_pk_fma_f32 v[210:211], v[240:241], v[210:211], v[66:67] op_sel:[1,0,0]
	v_pk_fma_f32 v[212:213], v[240:241], v[212:213], v[56:57] op_sel:[1,0,0]
	v_pk_fma_f32 v[214:215], v[240:241], v[214:215], v[58:59] op_sel:[1,0,0]
	v_pk_fma_f32 v[216:217], v[44:45], v[240:241], v[20:21] op_sel_hi:[1,0,1] neg_lo:[1,0,0] neg_hi:[1,0,0]
	v_pk_fma_f32 v[218:219], v[46:47], v[240:241], v[22:23] op_sel_hi:[1,0,1] neg_lo:[1,0,0] neg_hi:[1,0,0]
	v_pk_fma_f32 v[220:221], v[36:37], v[240:241], v[16:17] op_sel_hi:[1,0,1] neg_lo:[1,0,0] neg_hi:[1,0,0]
	v_pk_fma_f32 v[222:223], v[38:39], v[240:241], v[18:19] op_sel_hi:[1,0,1] neg_lo:[1,0,0] neg_hi:[1,0,0]
	v_pk_fma_f32 v[216:217], v[240:241], v[216:217], v[40:41] op_sel:[1,0,0]
	v_pk_fma_f32 v[218:219], v[240:241], v[218:219], v[42:43] op_sel:[1,0,0]
	v_pk_fma_f32 v[220:221], v[240:241], v[220:221], v[32:33] op_sel:[1,0,0]
	v_pk_fma_f32 v[222:223], v[240:241], v[222:223], v[34:35] op_sel:[1,0,0]
	v_pk_fma_f32 v[224:225], v[68:69], v[242:243], v[12:13] op_sel_hi:[1,0,1] neg_lo:[1,0,0] neg_hi:[1,0,0]
	v_pk_fma_f32 v[226:227], v[70:71], v[242:243], v[14:15] op_sel_hi:[1,0,1] neg_lo:[1,0,0] neg_hi:[1,0,0]
	v_pk_fma_f32 v[228:229], v[60:61], v[242:243], v[8:9] op_sel_hi:[1,0,1] neg_lo:[1,0,0] neg_hi:[1,0,0]
	v_pk_fma_f32 v[230:231], v[62:63], v[242:243], v[10:11] op_sel_hi:[1,0,1] neg_lo:[1,0,0] neg_hi:[1,0,0]
	v_pk_fma_f32 v[224:225], v[242:243], v[224:225], v[64:65] op_sel:[1,0,0]
	v_pk_fma_f32 v[226:227], v[242:243], v[226:227], v[66:67] op_sel:[1,0,0]
	v_pk_fma_f32 v[228:229], v[242:243], v[228:229], v[56:57] op_sel:[1,0,0]
	v_pk_fma_f32 v[230:231], v[242:243], v[230:231], v[58:59] op_sel:[1,0,0]
	v_pk_fma_f32 v[232:233], v[44:45], v[242:243], v[4:5] op_sel_hi:[1,0,1] neg_lo:[1,0,0] neg_hi:[1,0,0]
	v_pk_fma_f32 v[234:235], v[46:47], v[242:243], v[6:7] op_sel_hi:[1,0,1] neg_lo:[1,0,0] neg_hi:[1,0,0]
	v_pk_fma_f32 v[236:237], v[36:37], v[242:243], v[0:1] op_sel_hi:[1,0,1] neg_lo:[1,0,0] neg_hi:[1,0,0]
	v_pk_fma_f32 v[238:239], v[38:39], v[242:243], v[2:3] op_sel_hi:[1,0,1] neg_lo:[1,0,0] neg_hi:[1,0,0]
	v_pk_fma_f32 v[232:233], v[242:243], v[232:233], v[40:41] op_sel:[1,0,0]
	v_pk_fma_f32 v[234:235], v[242:243], v[234:235], v[42:43] op_sel:[1,0,0]
	v_pk_fma_f32 v[236:237], v[242:243], v[236:237], v[32:33] op_sel:[1,0,0]
	v_pk_fma_f32 v[238:239], v[242:243], v[238:239], v[34:35] op_sel:[1,0,0]
	v_mov_b32_e32 v248, s79
	v_mov_b32_e32 v249, s79
	s_mov_b32 s72, s70
	s_mov_b32 s73, s71
	s_mov_b32 s74, s69
	s_mov_b64 s[42:43], s[4:5]
	s_mov_b64 s[40:41], s[6:7]
	v_fma_f32 v242, |v176|, s80, 1.0
	v_fma_f32 v243, |v177|, s80, 1.0
	v_mul_f32_e32 v246, v176, v176
	v_rcp_f32_e32 v242, v242
	v_rcp_f32_e32 v243, v243
	v_mul_f32_e32 v247, v177, v177
	v_mul_f32_e32 v246, s90, v246
	v_mul_f32_e32 v247, s90, v247
	v_fma_f32 v244, v242, s82, v248
	v_fma_f32 v245, v243, s82, v248
	v_exp_f32_e32 v246, v246
	v_exp_f32_e32 v247, v247
	v_fmaak_f32 v244, v242, v244, 0x3f35f0e3
	v_fmaak_f32 v245, v243, v245, 0x3f35f0e3
	v_fmaak_f32 v244, v242, v244, 0xbe11a98e
	v_fmaak_f32 v245, v243, v245, 0xbe11a98e
	v_fmaak_f32 v244, v242, v244, 0x3e027906
	v_fmaak_f32 v245, v243, v245, 0x3e027906
	v_mul_f32_e32 v244, v242, v244
	v_mul_f32_e32 v245, v243, v245
	v_max_f32_e32 v242, 0, v176
	v_max_f32_e32 v243, 0, v177
	v_mul_f32_e32 v244, v244, v246
	v_mul_f32_e32 v245, v245, v247
	v_fma_f32 v244, -|v176|, v244, v242
	v_fma_f32 v245, -|v177|, v245, v243
	v_cvt_pk_f16_f32 v176, v244, v245
	v_fma_f32 v242, |v178|, s80, 1.0
	v_fma_f32 v243, |v179|, s80, 1.0
	v_mul_f32_e32 v246, v178, v178
	v_rcp_f32_e32 v242, v242
	v_rcp_f32_e32 v243, v243
	v_mul_f32_e32 v247, v179, v179
	v_mul_f32_e32 v246, s90, v246
	v_mul_f32_e32 v247, s90, v247
	v_fma_f32 v244, v242, s82, v248
	v_fma_f32 v245, v243, s82, v248
	v_exp_f32_e32 v246, v246
	v_exp_f32_e32 v247, v247
	v_fmaak_f32 v244, v242, v244, 0x3f35f0e3
	v_fmaak_f32 v245, v243, v245, 0x3f35f0e3
	v_fmaak_f32 v244, v242, v244, 0xbe11a98e
	v_fmaak_f32 v245, v243, v245, 0xbe11a98e
	v_fmaak_f32 v244, v242, v244, 0x3e027906
	v_fmaak_f32 v245, v243, v245, 0x3e027906
	v_mul_f32_e32 v244, v242, v244
	v_mul_f32_e32 v245, v243, v245
	v_max_f32_e32 v242, 0, v178
	v_max_f32_e32 v243, 0, v179
	v_mul_f32_e32 v244, v244, v246
	v_mul_f32_e32 v245, v245, v247
	v_fma_f32 v244, -|v178|, v244, v242
	v_fma_f32 v245, -|v179|, v245, v243
	v_cvt_pk_f16_f32 v177, v244, v245
	v_fma_f32 v242, |v180|, s80, 1.0
	v_fma_f32 v243, |v181|, s80, 1.0
	v_mul_f32_e32 v246, v180, v180
	v_rcp_f32_e32 v242, v242
	v_rcp_f32_e32 v243, v243
	v_mul_f32_e32 v247, v181, v181
	v_mul_f32_e32 v246, s90, v246
	v_mul_f32_e32 v247, s90, v247
	v_fma_f32 v244, v242, s82, v248
	v_fma_f32 v245, v243, s82, v248
	v_exp_f32_e32 v246, v246
	v_exp_f32_e32 v247, v247
	v_fmaak_f32 v244, v242, v244, 0x3f35f0e3
	v_fmaak_f32 v245, v243, v245, 0x3f35f0e3
	v_fmaak_f32 v244, v242, v244, 0xbe11a98e
	v_fmaak_f32 v245, v243, v245, 0xbe11a98e
	v_fmaak_f32 v244, v242, v244, 0x3e027906
	v_fmaak_f32 v245, v243, v245, 0x3e027906
	v_mul_f32_e32 v244, v242, v244
	v_mul_f32_e32 v245, v243, v245
	v_max_f32_e32 v242, 0, v180
	v_max_f32_e32 v243, 0, v181
	v_mul_f32_e32 v244, v244, v246
	v_mul_f32_e32 v245, v245, v247
	v_fma_f32 v244, -|v180|, v244, v242
	v_fma_f32 v245, -|v181|, v245, v243
	v_cvt_pk_f16_f32 v178, v244, v245
	v_fma_f32 v242, |v182|, s80, 1.0
	v_fma_f32 v243, |v183|, s80, 1.0
	v_mul_f32_e32 v246, v182, v182
	v_rcp_f32_e32 v242, v242
	v_rcp_f32_e32 v243, v243
	v_mul_f32_e32 v247, v183, v183
	v_mul_f32_e32 v246, s90, v246
	v_mul_f32_e32 v247, s90, v247
	v_fma_f32 v244, v242, s82, v248
	v_fma_f32 v245, v243, s82, v248
	v_exp_f32_e32 v246, v246
	v_exp_f32_e32 v247, v247
	v_fmaak_f32 v244, v242, v244, 0x3f35f0e3
	v_fmaak_f32 v245, v243, v245, 0x3f35f0e3
	v_fmaak_f32 v244, v242, v244, 0xbe11a98e
	v_fmaak_f32 v245, v243, v245, 0xbe11a98e
	v_fmaak_f32 v244, v242, v244, 0x3e027906
	v_fmaak_f32 v245, v243, v245, 0x3e027906
	v_mul_f32_e32 v244, v242, v244
	v_mul_f32_e32 v245, v243, v245
	v_max_f32_e32 v242, 0, v182
	v_max_f32_e32 v243, 0, v183
	v_mul_f32_e32 v244, v244, v246
	v_mul_f32_e32 v245, v245, v247
	v_fma_f32 v244, -|v182|, v244, v242
	v_fma_f32 v245, -|v183|, v245, v243
	v_cvt_pk_f16_f32 v179, v244, v245
	global_store_dwordx4 v[250:251], v[176:179], off sc1
	v_fma_f32 v242, |v192|, s80, 1.0
	v_fma_f32 v243, |v193|, s80, 1.0
	v_mul_f32_e32 v246, v192, v192
	v_rcp_f32_e32 v242, v242
	v_rcp_f32_e32 v243, v243
	v_mul_f32_e32 v247, v193, v193
	v_mul_f32_e32 v246, s90, v246
	v_mul_f32_e32 v247, s90, v247
	v_fma_f32 v244, v242, s82, v248
	v_fma_f32 v245, v243, s82, v248
	v_exp_f32_e32 v246, v246
	v_exp_f32_e32 v247, v247
	v_fmaak_f32 v244, v242, v244, 0x3f35f0e3
	v_fmaak_f32 v245, v243, v245, 0x3f35f0e3
	v_fmaak_f32 v244, v242, v244, 0xbe11a98e
	v_fmaak_f32 v245, v243, v245, 0xbe11a98e
	v_fmaak_f32 v244, v242, v244, 0x3e027906
	v_fmaak_f32 v245, v243, v245, 0x3e027906
	v_mul_f32_e32 v244, v242, v244
	v_mul_f32_e32 v245, v243, v245
	v_max_f32_e32 v242, 0, v192
	v_max_f32_e32 v243, 0, v193
	v_mul_f32_e32 v244, v244, v246
	v_mul_f32_e32 v245, v245, v247
	v_fma_f32 v244, -|v192|, v244, v242
	v_fma_f32 v245, -|v193|, v245, v243
	v_cvt_pk_f16_f32 v192, v244, v245
	v_fma_f32 v242, |v194|, s80, 1.0
	v_fma_f32 v243, |v195|, s80, 1.0
	v_mul_f32_e32 v246, v194, v194
	v_rcp_f32_e32 v242, v242
	v_rcp_f32_e32 v243, v243
	v_mul_f32_e32 v247, v195, v195
	v_mul_f32_e32 v246, s90, v246
	v_mul_f32_e32 v247, s90, v247
	v_fma_f32 v244, v242, s82, v248
	v_fma_f32 v245, v243, s82, v248
	v_exp_f32_e32 v246, v246
	v_exp_f32_e32 v247, v247
	v_fmaak_f32 v244, v242, v244, 0x3f35f0e3
	v_fmaak_f32 v245, v243, v245, 0x3f35f0e3
	v_fmaak_f32 v244, v242, v244, 0xbe11a98e
	v_fmaak_f32 v245, v243, v245, 0xbe11a98e
	v_fmaak_f32 v244, v242, v244, 0x3e027906
	v_fmaak_f32 v245, v243, v245, 0x3e027906
	v_mul_f32_e32 v244, v242, v244
	v_mul_f32_e32 v245, v243, v245
	v_max_f32_e32 v242, 0, v194
	v_max_f32_e32 v243, 0, v195
	v_mul_f32_e32 v244, v244, v246
	v_mul_f32_e32 v245, v245, v247
	v_fma_f32 v244, -|v194|, v244, v242
	v_fma_f32 v245, -|v195|, v245, v243
	v_cvt_pk_f16_f32 v193, v244, v245
	v_fma_f32 v242, |v196|, s80, 1.0
	v_fma_f32 v243, |v197|, s80, 1.0
	v_mul_f32_e32 v246, v196, v196
	v_rcp_f32_e32 v242, v242
	v_rcp_f32_e32 v243, v243
	v_mul_f32_e32 v247, v197, v197
	v_mul_f32_e32 v246, s90, v246
	v_mul_f32_e32 v247, s90, v247
	v_fma_f32 v244, v242, s82, v248
	v_fma_f32 v245, v243, s82, v248
	v_exp_f32_e32 v246, v246
	v_exp_f32_e32 v247, v247
	v_fmaak_f32 v244, v242, v244, 0x3f35f0e3
	v_fmaak_f32 v245, v243, v245, 0x3f35f0e3
	v_fmaak_f32 v244, v242, v244, 0xbe11a98e
	v_fmaak_f32 v245, v243, v245, 0xbe11a98e
	v_fmaak_f32 v244, v242, v244, 0x3e027906
	v_fmaak_f32 v245, v243, v245, 0x3e027906
	v_mul_f32_e32 v244, v242, v244
	v_mul_f32_e32 v245, v243, v245
	v_max_f32_e32 v242, 0, v196
	v_max_f32_e32 v243, 0, v197
	v_mul_f32_e32 v244, v244, v246
	v_mul_f32_e32 v245, v245, v247
	v_fma_f32 v244, -|v196|, v244, v242
	v_fma_f32 v245, -|v197|, v245, v243
	v_cvt_pk_f16_f32 v194, v244, v245
	v_fma_f32 v242, |v198|, s80, 1.0
	v_fma_f32 v243, |v199|, s80, 1.0
	v_mul_f32_e32 v246, v198, v198
	v_rcp_f32_e32 v242, v242
	v_rcp_f32_e32 v243, v243
	v_mul_f32_e32 v247, v199, v199
	v_mul_f32_e32 v246, s90, v246
	v_mul_f32_e32 v247, s90, v247
	v_fma_f32 v244, v242, s82, v248
	v_fma_f32 v245, v243, s82, v248
	v_exp_f32_e32 v246, v246
	v_exp_f32_e32 v247, v247
	v_fmaak_f32 v244, v242, v244, 0x3f35f0e3
	v_fmaak_f32 v245, v243, v245, 0x3f35f0e3
	v_fmaak_f32 v244, v242, v244, 0xbe11a98e
	v_fmaak_f32 v245, v243, v245, 0xbe11a98e
	v_fmaak_f32 v244, v242, v244, 0x3e027906
	v_fmaak_f32 v245, v243, v245, 0x3e027906
	v_mul_f32_e32 v244, v242, v244
	v_mul_f32_e32 v245, v243, v245
	v_max_f32_e32 v242, 0, v198
	v_max_f32_e32 v243, 0, v199
	v_mul_f32_e32 v244, v244, v246
	v_mul_f32_e32 v245, v245, v247
	v_fma_f32 v244, -|v198|, v244, v242
	v_fma_f32 v245, -|v199|, v245, v243
	v_cvt_pk_f16_f32 v195, v244, v245
	v_lshl_add_u64 v[252:253], v[250:251], 0, s[92:93]
	global_store_dwordx4 v[252:253], v[192:195], off sc1
	v_fma_f32 v242, |v208|, s80, 1.0
	v_fma_f32 v243, |v209|, s80, 1.0
	v_mul_f32_e32 v246, v208, v208
	v_rcp_f32_e32 v242, v242
	v_rcp_f32_e32 v243, v243
	v_mul_f32_e32 v247, v209, v209
	v_mul_f32_e32 v246, s90, v246
	v_mul_f32_e32 v247, s90, v247
	v_fma_f32 v244, v242, s82, v248
	v_fma_f32 v245, v243, s82, v248
	v_exp_f32_e32 v246, v246
	v_exp_f32_e32 v247, v247
	v_fmaak_f32 v244, v242, v244, 0x3f35f0e3
	v_fmaak_f32 v245, v243, v245, 0x3f35f0e3
	v_fmaak_f32 v244, v242, v244, 0xbe11a98e
	v_fmaak_f32 v245, v243, v245, 0xbe11a98e
	v_fmaak_f32 v244, v242, v244, 0x3e027906
	v_fmaak_f32 v245, v243, v245, 0x3e027906
	v_mul_f32_e32 v244, v242, v244
	v_mul_f32_e32 v245, v243, v245
	v_max_f32_e32 v242, 0, v208
	v_max_f32_e32 v243, 0, v209
	v_mul_f32_e32 v244, v244, v246
	v_mul_f32_e32 v245, v245, v247
	v_fma_f32 v244, -|v208|, v244, v242
	v_fma_f32 v245, -|v209|, v245, v243
	v_cvt_pk_f16_f32 v208, v244, v245
	v_fma_f32 v242, |v210|, s80, 1.0
	v_fma_f32 v243, |v211|, s80, 1.0
	v_mul_f32_e32 v246, v210, v210
	v_rcp_f32_e32 v242, v242
	v_rcp_f32_e32 v243, v243
	v_mul_f32_e32 v247, v211, v211
	v_mul_f32_e32 v246, s90, v246
	v_mul_f32_e32 v247, s90, v247
	v_fma_f32 v244, v242, s82, v248
	v_fma_f32 v245, v243, s82, v248
	v_exp_f32_e32 v246, v246
	v_exp_f32_e32 v247, v247
	v_fmaak_f32 v244, v242, v244, 0x3f35f0e3
	v_fmaak_f32 v245, v243, v245, 0x3f35f0e3
	v_fmaak_f32 v244, v242, v244, 0xbe11a98e
	v_fmaak_f32 v245, v243, v245, 0xbe11a98e
	v_fmaak_f32 v244, v242, v244, 0x3e027906
	v_fmaak_f32 v245, v243, v245, 0x3e027906
	v_mul_f32_e32 v244, v242, v244
	v_mul_f32_e32 v245, v243, v245
	v_max_f32_e32 v242, 0, v210
	v_max_f32_e32 v243, 0, v211
	v_mul_f32_e32 v244, v244, v246
	v_mul_f32_e32 v245, v245, v247
	v_fma_f32 v244, -|v210|, v244, v242
	v_fma_f32 v245, -|v211|, v245, v243
	v_cvt_pk_f16_f32 v209, v244, v245
	v_fma_f32 v242, |v212|, s80, 1.0
	v_fma_f32 v243, |v213|, s80, 1.0
	v_mul_f32_e32 v246, v212, v212
	v_rcp_f32_e32 v242, v242
	v_rcp_f32_e32 v243, v243
	v_mul_f32_e32 v247, v213, v213
	v_mul_f32_e32 v246, s90, v246
	v_mul_f32_e32 v247, s90, v247
	v_fma_f32 v244, v242, s82, v248
	v_fma_f32 v245, v243, s82, v248
	v_exp_f32_e32 v246, v246
	v_exp_f32_e32 v247, v247
	v_fmaak_f32 v244, v242, v244, 0x3f35f0e3
	v_fmaak_f32 v245, v243, v245, 0x3f35f0e3
	v_fmaak_f32 v244, v242, v244, 0xbe11a98e
	v_fmaak_f32 v245, v243, v245, 0xbe11a98e
	v_fmaak_f32 v244, v242, v244, 0x3e027906
	v_fmaak_f32 v245, v243, v245, 0x3e027906
	v_mul_f32_e32 v244, v242, v244
	v_mul_f32_e32 v245, v243, v245
	v_max_f32_e32 v242, 0, v212
	v_max_f32_e32 v243, 0, v213
	v_mul_f32_e32 v244, v244, v246
	v_mul_f32_e32 v245, v245, v247
	v_fma_f32 v244, -|v212|, v244, v242
	v_fma_f32 v245, -|v213|, v245, v243
	v_cvt_pk_f16_f32 v210, v244, v245
	v_fma_f32 v242, |v214|, s80, 1.0
	v_fma_f32 v243, |v215|, s80, 1.0
	v_mul_f32_e32 v246, v214, v214
	v_rcp_f32_e32 v242, v242
	v_rcp_f32_e32 v243, v243
	v_mul_f32_e32 v247, v215, v215
	v_mul_f32_e32 v246, s90, v246
	v_mul_f32_e32 v247, s90, v247
	v_fma_f32 v244, v242, s82, v248
	v_fma_f32 v245, v243, s82, v248
	v_exp_f32_e32 v246, v246
	v_exp_f32_e32 v247, v247
	v_fmaak_f32 v244, v242, v244, 0x3f35f0e3
	v_fmaak_f32 v245, v243, v245, 0x3f35f0e3
	v_fmaak_f32 v244, v242, v244, 0xbe11a98e
	v_fmaak_f32 v245, v243, v245, 0xbe11a98e
	v_fmaak_f32 v244, v242, v244, 0x3e027906
	v_fmaak_f32 v245, v243, v245, 0x3e027906
	v_mul_f32_e32 v244, v242, v244
	v_mul_f32_e32 v245, v243, v245
	v_max_f32_e32 v242, 0, v214
	v_max_f32_e32 v243, 0, v215
	v_mul_f32_e32 v244, v244, v246
	v_mul_f32_e32 v245, v245, v247
	v_fma_f32 v244, -|v214|, v244, v242
	v_fma_f32 v245, -|v215|, v245, v243
	v_cvt_pk_f16_f32 v211, v244, v245
	v_lshl_add_u64 v[252:253], v[250:251], 0, s[94:95]
	global_store_dwordx4 v[252:253], v[208:211], off sc1
	v_fma_f32 v242, |v224|, s80, 1.0
	v_fma_f32 v243, |v225|, s80, 1.0
	v_mul_f32_e32 v246, v224, v224
	v_rcp_f32_e32 v242, v242
	v_rcp_f32_e32 v243, v243
	v_mul_f32_e32 v247, v225, v225
	v_mul_f32_e32 v246, s90, v246
	v_mul_f32_e32 v247, s90, v247
	v_fma_f32 v244, v242, s82, v248
	v_fma_f32 v245, v243, s82, v248
	v_exp_f32_e32 v246, v246
	v_exp_f32_e32 v247, v247
	v_fmaak_f32 v244, v242, v244, 0x3f35f0e3
	v_fmaak_f32 v245, v243, v245, 0x3f35f0e3
	v_fmaak_f32 v244, v242, v244, 0xbe11a98e
	v_fmaak_f32 v245, v243, v245, 0xbe11a98e
	v_fmaak_f32 v244, v242, v244, 0x3e027906
	v_fmaak_f32 v245, v243, v245, 0x3e027906
	v_mul_f32_e32 v244, v242, v244
	v_mul_f32_e32 v245, v243, v245
	v_max_f32_e32 v242, 0, v224
	v_max_f32_e32 v243, 0, v225
	v_mul_f32_e32 v244, v244, v246
	v_mul_f32_e32 v245, v245, v247
	v_fma_f32 v244, -|v224|, v244, v242
	v_fma_f32 v245, -|v225|, v245, v243
	v_cvt_pk_f16_f32 v224, v244, v245
	v_fma_f32 v242, |v226|, s80, 1.0
	v_fma_f32 v243, |v227|, s80, 1.0
	v_mul_f32_e32 v246, v226, v226
	v_rcp_f32_e32 v242, v242
	v_rcp_f32_e32 v243, v243
	v_mul_f32_e32 v247, v227, v227
	v_mul_f32_e32 v246, s90, v246
	v_mul_f32_e32 v247, s90, v247
	v_fma_f32 v244, v242, s82, v248
	v_fma_f32 v245, v243, s82, v248
	v_exp_f32_e32 v246, v246
	v_exp_f32_e32 v247, v247
	v_fmaak_f32 v244, v242, v244, 0x3f35f0e3
	v_fmaak_f32 v245, v243, v245, 0x3f35f0e3
	v_fmaak_f32 v244, v242, v244, 0xbe11a98e
	v_fmaak_f32 v245, v243, v245, 0xbe11a98e
	v_fmaak_f32 v244, v242, v244, 0x3e027906
	v_fmaak_f32 v245, v243, v245, 0x3e027906
	v_mul_f32_e32 v244, v242, v244
	v_mul_f32_e32 v245, v243, v245
	v_max_f32_e32 v242, 0, v226
	v_max_f32_e32 v243, 0, v227
	v_mul_f32_e32 v244, v244, v246
	v_mul_f32_e32 v245, v245, v247
	v_fma_f32 v244, -|v226|, v244, v242
	v_fma_f32 v245, -|v227|, v245, v243
	v_cvt_pk_f16_f32 v225, v244, v245
	v_fma_f32 v242, |v228|, s80, 1.0
	v_fma_f32 v243, |v229|, s80, 1.0
	v_mul_f32_e32 v246, v228, v228
	v_rcp_f32_e32 v242, v242
	v_rcp_f32_e32 v243, v243
	v_mul_f32_e32 v247, v229, v229
	v_mul_f32_e32 v246, s90, v246
	v_mul_f32_e32 v247, s90, v247
	v_fma_f32 v244, v242, s82, v248
	v_fma_f32 v245, v243, s82, v248
	v_exp_f32_e32 v246, v246
	v_exp_f32_e32 v247, v247
	v_fmaak_f32 v244, v242, v244, 0x3f35f0e3
	v_fmaak_f32 v245, v243, v245, 0x3f35f0e3
	v_fmaak_f32 v244, v242, v244, 0xbe11a98e
	v_fmaak_f32 v245, v243, v245, 0xbe11a98e
	v_fmaak_f32 v244, v242, v244, 0x3e027906
	v_fmaak_f32 v245, v243, v245, 0x3e027906
	v_mul_f32_e32 v244, v242, v244
	v_mul_f32_e32 v245, v243, v245
	v_max_f32_e32 v242, 0, v228
	v_max_f32_e32 v243, 0, v229
	v_mul_f32_e32 v244, v244, v246
	v_mul_f32_e32 v245, v245, v247
	v_fma_f32 v244, -|v228|, v244, v242
	v_fma_f32 v245, -|v229|, v245, v243
	v_cvt_pk_f16_f32 v226, v244, v245
	v_fma_f32 v242, |v230|, s80, 1.0
	v_fma_f32 v243, |v231|, s80, 1.0
	v_mul_f32_e32 v246, v230, v230
	v_rcp_f32_e32 v242, v242
	v_rcp_f32_e32 v243, v243
	v_mul_f32_e32 v247, v231, v231
	v_mul_f32_e32 v246, s90, v246
	v_mul_f32_e32 v247, s90, v247
	v_fma_f32 v244, v242, s82, v248
	v_fma_f32 v245, v243, s82, v248
	v_exp_f32_e32 v246, v246
	v_exp_f32_e32 v247, v247
	v_fmaak_f32 v244, v242, v244, 0x3f35f0e3
	v_fmaak_f32 v245, v243, v245, 0x3f35f0e3
	v_fmaak_f32 v244, v242, v244, 0xbe11a98e
	v_fmaak_f32 v245, v243, v245, 0xbe11a98e
	v_fmaak_f32 v244, v242, v244, 0x3e027906
	v_fmaak_f32 v245, v243, v245, 0x3e027906
	v_mul_f32_e32 v244, v242, v244
	v_mul_f32_e32 v245, v243, v245
	v_max_f32_e32 v242, 0, v230
	v_max_f32_e32 v243, 0, v231
	v_mul_f32_e32 v244, v244, v246
	v_mul_f32_e32 v245, v245, v247
	v_fma_f32 v244, -|v230|, v244, v242
	v_fma_f32 v245, -|v231|, v245, v243
	v_cvt_pk_f16_f32 v227, v244, v245
	v_lshl_add_u64 v[252:253], v[250:251], 0, s[96:97]
	global_store_dwordx4 v[252:253], v[224:227], off sc1
	s_mov_b32 s78, 1
	s_branch .LBB5_43

.Lg_loop:
	s_add_u32 s46, s40, s44
	s_addc_u32 s47, s41, s45
	s_add_u32 s46, s46, 0x180
	s_addc_u32 s47, s47, 0
	s_add_u32 s48, s42, s44
	s_addc_u32 s49, s43, s45
	s_add_u32 s76, s48, 0x180
	s_addc_u32 s77, s49, 0
	s_cmp_eq_u32 s67, s75
	s_cselect_b32 s49, s7, s47
	s_cselect_b32 s48, s6, s46
	s_cselect_b32 s47, s5, s77
	s_cselect_b32 s46, s4, s76
	s_add_i32 s76, s19, s54
	v_lshl_add_u64 v[126:127], v[32:33], 0, s[44:45]
	s_mov_b32 m0, s76
	ds_read_b128 v[44:47], v130 offset:16384
	ds_read_b128 v[56:59], v130 offset:17408
	ds_read_b128 v[60:63], v130 offset:18432
	ds_read_b128 v[64:67], v130 offset:19456
	ds_read_b128 v[68:71], v131
	ds_read_b128 v[96:99], v131 offset:1024
	ds_read_b128 v[136:139], v131 offset:2048
	ds_read_b128 v[140:143], v131 offset:3072
	ds_read_b128 v[144:147], v131 offset:4096
	ds_read_b128 v[148:151], v131 offset:5120
	ds_read_b128 v[152:155], v131 offset:6144
	ds_read_b128 v[156:159], v131 offset:7168
	global_load_lds_dwordx4 v[126:127], off
	v_lshl_add_u64 v[126:127], v[34:35], 0, s[44:45]
	s_add_i32 m0, s76, 0x2000
	s_add_i32 s76, s27, s54
	global_load_lds_dwordx4 v[126:127], off
	v_lshl_add_u64 v[126:127], v[36:37], 0, s[44:45]
	s_mov_b32 m0, s76
	s_nop 0
	global_load_lds_dwordx4 v[126:127], off
	v_lshl_add_u64 v[126:127], v[38:39], 0, s[44:45]
	s_add_i32 m0, s76, 0x2000
	s_nop 0
	global_load_lds_dwordx4 v[126:127], off
	s_barrier
	s_waitcnt lgkmcnt(0)
	s_setprio 1
	s_waitcnt lgkmcnt(0)
	v_mfma_f32_16x16x32_f16 v[92:95], v[44:47], v[68:71], v[92:95]
	v_fma_f32 v242, |v184|, s80, 1.0
	v_fma_f32 v243, |v185|, s80, 1.0
	v_mfma_f32_16x16x32_f16 v[88:91], v[60:63], v[68:71], v[88:91]
	v_mul_f32_e32 v246, v184, v184
	v_mfma_f32_16x16x32_f16 v[76:79], v[44:47], v[136:139], v[76:79]
	v_rcp_f32_e32 v242, v242
	v_mfma_f32_16x16x32_f16 v[72:75], v[60:63], v[136:139], v[72:75]
	v_rcp_f32_e32 v243, v243
	v_mfma_f32_16x16x32_f16 v[28:31], v[44:47], v[144:147], v[28:31]
	v_mul_f32_e32 v247, v185, v185
	v_mfma_f32_16x16x32_f16 v[24:27], v[60:63], v[144:147], v[24:27]
	v_mul_f32_e32 v246, s90, v246
	v_mul_f32_e32 v247, s90, v247
	v_mfma_f32_16x16x32_f16 v[12:15], v[44:47], v[152:155], v[12:15]
	v_fma_f32 v244, v242, s82, v248
	v_mfma_f32_16x16x32_f16 v[8:11], v[60:63], v[152:155], v[8:11]
	v_fma_f32 v245, v243, s82, v248
	v_mfma_f32_16x16x32_f16 v[92:95], v[56:59], v[96:99], v[92:95]
	v_exp_f32_e32 v246, v246
	v_mfma_f32_16x16x32_f16 v[88:91], v[64:67], v[96:99], v[88:91]
	v_exp_f32_e32 v247, v247
	v_mfma_f32_16x16x32_f16 v[76:79], v[56:59], v[140:143], v[76:79]
	v_fmaak_f32 v244, v242, v244, 0x3f35f0e3
	v_mfma_f32_16x16x32_f16 v[72:75], v[64:67], v[140:143], v[72:75]
	v_fmaak_f32 v245, v243, v245, 0x3f35f0e3
	v_fmaak_f32 v244, v242, v244, 0xbe11a98e
	v_mfma_f32_16x16x32_f16 v[28:31], v[56:59], v[148:151], v[28:31]
	v_fmaak_f32 v245, v243, v245, 0xbe11a98e
	v_mfma_f32_16x16x32_f16 v[24:27], v[64:67], v[148:151], v[24:27]
	v_fmaak_f32 v244, v242, v244, 0x3e027906
	v_mfma_f32_16x16x32_f16 v[12:15], v[56:59], v[156:159], v[12:15]
	v_fmaak_f32 v245, v243, v245, 0x3e027906
	v_mfma_f32_16x16x32_f16 v[8:11], v[64:67], v[156:159], v[8:11]
	v_mul_f32_e32 v244, v242, v244
	s_setprio 0
	s_barrier
	s_add_i32 s76, s68, s54
	v_lshl_add_u64 v[126:127], v[40:41], 0, s[44:45]
	s_mov_b32 m0, s76
	ds_read_b128 v[44:47], v130 offset:32768
	ds_read_b128 v[56:59], v130 offset:33792
	ds_read_b128 v[60:63], v130 offset:34816
	ds_read_b128 v[64:67], v130 offset:35840
	global_load_lds_dwordx4 v[126:127], off
	v_lshl_add_u64 v[126:127], v[42:43], 0, s[44:45]
	s_add_i32 m0, s76, 0x2000
	s_nop 0
	global_load_lds_dwordx4 v[126:127], off
	s_waitcnt vmcnt(6)
	s_barrier
	s_waitcnt lgkmcnt(0)
	s_setprio 1
	s_waitcnt lgkmcnt(0)
	v_mfma_f32_16x16x32_f16 v[84:87], v[44:47], v[68:71], v[84:87]
	v_mul_f32_e32 v245, v243, v245
	v_mfma_f32_16x16x32_f16 v[52:55], v[44:47], v[136:139], v[52:55]
	v_max_f32_e32 v242, 0, v184
	v_max_f32_e32 v243, 0, v185
	v_mfma_f32_16x16x32_f16 v[48:51], v[60:63], v[136:139], v[48:51]
	v_mul_f32_e32 v244, v244, v246
	v_mfma_f32_16x16x32_f16 v[20:23], v[44:47], v[144:147], v[20:23]
	v_mul_f32_e32 v245, v245, v247
	v_mfma_f32_16x16x32_f16 v[16:19], v[60:63], v[144:147], v[16:19]
	v_fma_f32 v244, -|v184|, v244, v242
	v_mfma_f32_16x16x32_f16 v[4:7], v[44:47], v[152:155], v[4:7]
	v_fma_f32 v245, -|v185|, v245, v243
	v_mfma_f32_16x16x32_f16 v[0:3], v[60:63], v[152:155], v[0:3]
	v_cvt_pk_f16_f32 v184, v244, v245
	v_mfma_f32_16x16x32_f16 v[84:87], v[56:59], v[96:99], v[84:87]
	v_fma_f32 v242, |v186|, s80, 1.0
	v_fma_f32 v243, |v187|, s80, 1.0
	v_mfma_f32_16x16x32_f16 v[68:71], v[60:63], v[68:71], v[80:83]
	v_mul_f32_e32 v246, v186, v186
	v_mfma_f32_16x16x32_f16 v[52:55], v[56:59], v[140:143], v[52:55]
	v_rcp_f32_e32 v242, v242
	v_mfma_f32_16x16x32_f16 v[48:51], v[64:67], v[140:143], v[48:51]
	v_rcp_f32_e32 v243, v243
	v_mfma_f32_16x16x32_f16 v[20:23], v[56:59], v[148:151], v[20:23]
	v_mul_f32_e32 v247, v187, v187
	v_mfma_f32_16x16x32_f16 v[16:19], v[64:67], v[148:151], v[16:19]
	v_mul_f32_e32 v246, s90, v246
	v_mfma_f32_16x16x32_f16 v[4:7], v[56:59], v[156:159], v[4:7]
	v_mul_f32_e32 v247, s90, v247
	v_fma_f32 v244, v242, s82, v248
	v_mfma_f32_16x16x32_f16 v[0:3], v[64:67], v[156:159], v[0:3]
	v_fma_f32 v245, v243, s82, v248
	v_mfma_f32_16x16x32_f16 v[68:71], v[64:67], v[96:99], v[68:71]
	v_exp_f32_e32 v246, v246
	s_setprio 0
	s_barrier
	s_add_i32 s76, 0, 0x10000
	s_mov_b32 m0, s57
	v_add_u32_e32 v64, s76, v128
	v_lshl_add_u64 v[126:127], s[48:49], 0, v[100:101]
	ds_read_b128 v[44:47], v64
	ds_read_b128 v[56:59], v64 offset:1024
	ds_read_b128 v[60:63], v64 offset:2048
	ds_read_b128 v[64:67], v64 offset:3072
	ds_read_b128 v[80:83], v131 offset:49152
	ds_read_b128 v[96:99], v131 offset:50176
	ds_read_b128 v[136:139], v131 offset:51200
	ds_read_b128 v[140:143], v131 offset:52224
	ds_read_b128 v[144:147], v131 offset:53248
	ds_read_b128 v[148:151], v131 offset:54272
	ds_read_b128 v[152:155], v131 offset:55296
	ds_read_b128 v[156:159], v131 offset:56320
	global_load_lds_dwordx4 v[126:127], off
	v_lshl_add_u64 v[160:161], s[48:49], 0, v[104:105]
	s_mov_b32 m0, s58
	v_lshl_add_u64 v[162:163], s[46:47], 0, v[102:103]
	global_load_lds_dwordx4 v[160:161], off
	s_mov_b32 m0, s59
	v_lshl_add_u64 v[164:165], s[46:47], 0, v[106:107]
	global_load_lds_dwordx4 v[162:163], off
	s_mov_b32 m0, s60
	s_nop 0
	global_load_lds_dwordx4 v[164:165], off
	s_barrier
	s_waitcnt lgkmcnt(0)
	s_setprio 1
	s_waitcnt lgkmcnt(0)
	v_mfma_f32_16x16x32_f16 v[92:95], v[44:47], v[80:83], v[92:95]
	v_exp_f32_e32 v247, v247
	v_mfma_f32_16x16x32_f16 v[88:91], v[60:63], v[80:83], v[88:91]
	v_fmaak_f32 v244, v242, v244, 0x3f35f0e3
	v_mfma_f32_16x16x32_f16 v[76:79], v[44:47], v[136:139], v[76:79]
	v_fmaak_f32 v245, v243, v245, 0x3f35f0e3
	v_mfma_f32_16x16x32_f16 v[72:75], v[60:63], v[136:139], v[72:75]
	v_fmaak_f32 v244, v242, v244, 0xbe11a98e
	v_fmaak_f32 v245, v243, v245, 0xbe11a98e
	v_mfma_f32_16x16x32_f16 v[28:31], v[44:47], v[144:147], v[28:31]
	v_fmaak_f32 v244, v242, v244, 0x3e027906
	v_mfma_f32_16x16x32_f16 v[24:27], v[60:63], v[144:147], v[24:27]
	v_fmaak_f32 v245, v243, v245, 0x3e027906
	v_mfma_f32_16x16x32_f16 v[12:15], v[44:47], v[152:155], v[12:15]
	v_mul_f32_e32 v244, v242, v244
	v_mfma_f32_16x16x32_f16 v[8:11], v[60:63], v[152:155], v[8:11]
	v_mul_f32_e32 v245, v243, v245
	v_mfma_f32_16x16x32_f16 v[92:95], v[56:59], v[96:99], v[92:95]
	v_max_f32_e32 v242, 0, v186
	v_mfma_f32_16x16x32_f16 v[88:91], v[64:67], v[96:99], v[88:91]
	v_max_f32_e32 v243, 0, v187
	v_mul_f32_e32 v244, v244, v246
	v_mfma_f32_16x16x32_f16 v[76:79], v[56:59], v[140:143], v[76:79]
	v_mul_f32_e32 v245, v245, v247
	v_mfma_f32_16x16x32_f16 v[72:75], v[64:67], v[140:143], v[72:75]
	v_fma_f32 v244, -|v186|, v244, v242
	v_mfma_f32_16x16x32_f16 v[28:31], v[56:59], v[148:151], v[28:31]
	v_fma_f32 v245, -|v187|, v245, v243
	v_mfma_f32_16x16x32_f16 v[24:27], v[64:67], v[148:151], v[24:27]
	v_cvt_pk_f16_f32 v185, v244, v245
	v_mfma_f32_16x16x32_f16 v[12:15], v[56:59], v[156:159], v[12:15]
	v_fma_f32 v242, |v188|, s80, 1.0
	v_mfma_f32_16x16x32_f16 v[8:11], v[64:67], v[156:159], v[8:11]
	v_fma_f32 v243, |v189|, s80, 1.0
	v_mul_f32_e32 v246, v188, v188
	s_setprio 0
	s_barrier
	s_add_i32 s48, 0, 0x14000
	s_add_u32 s46, s46, s10
	s_addc_u32 s47, s47, s11
	s_mov_b32 m0, s61
	v_add_u32_e32 v64, s48, v128
	v_lshl_add_u64 v[166:167], s[46:47], 0, v[102:103]
	ds_read_b128 v[44:47], v64
	ds_read_b128 v[56:59], v64 offset:1024
	ds_read_b128 v[60:63], v64 offset:2048
	ds_read_b128 v[64:67], v64 offset:3072
	global_load_lds_dwordx4 v[166:167], off
	v_lshl_add_u64 v[168:169], s[46:47], 0, v[106:107]
	s_mov_b32 m0, s62
	s_nop 0
	global_load_lds_dwordx4 v[168:169], off
	s_waitcnt vmcnt(6)
	s_barrier
	s_waitcnt lgkmcnt(0)
	s_setprio 1
	s_waitcnt lgkmcnt(0)
	v_mfma_f32_16x16x32_f16 v[84:87], v[44:47], v[80:83], v[84:87]
	v_rcp_f32_e32 v242, v242
	v_mfma_f32_16x16x32_f16 v[52:55], v[44:47], v[136:139], v[52:55]
	v_rcp_f32_e32 v243, v243
	v_mfma_f32_16x16x32_f16 v[48:51], v[60:63], v[136:139], v[48:51]
	v_mul_f32_e32 v247, v189, v189
	v_mfma_f32_16x16x32_f16 v[20:23], v[44:47], v[144:147], v[20:23]
	v_mul_f32_e32 v246, s90, v246
	v_mfma_f32_16x16x32_f16 v[16:19], v[60:63], v[144:147], v[16:19]
	v_mul_f32_e32 v247, s90, v247
	v_mfma_f32_16x16x32_f16 v[4:7], v[44:47], v[152:155], v[4:7]
	v_fma_f32 v244, v242, s82, v248
	v_fma_f32 v245, v243, s82, v248
	v_mfma_f32_16x16x32_f16 v[0:3], v[60:63], v[152:155], v[0:3]
	v_exp_f32_e32 v246, v246
	v_mfma_f32_16x16x32_f16 v[84:87], v[56:59], v[96:99], v[84:87]
	v_exp_f32_e32 v247, v247
	v_mfma_f32_16x16x32_f16 v[68:71], v[60:63], v[80:83], v[68:71]
	v_fmaak_f32 v244, v242, v244, 0x3f35f0e3
	v_mfma_f32_16x16x32_f16 v[52:55], v[56:59], v[140:143], v[52:55]
	v_fmaak_f32 v245, v243, v245, 0x3f35f0e3
	v_mfma_f32_16x16x32_f16 v[48:51], v[64:67], v[140:143], v[48:51]
	v_fmaak_f32 v244, v242, v244, 0xbe11a98e
	v_mfma_f32_16x16x32_f16 v[20:23], v[56:59], v[148:151], v[20:23]
	v_fmaak_f32 v245, v243, v245, 0xbe11a98e
	v_fmaak_f32 v244, v242, v244, 0x3e027906
	v_mfma_f32_16x16x32_f16 v[16:19], v[64:67], v[148:151], v[16:19]
	v_fmaak_f32 v245, v243, v245, 0x3e027906
	v_mfma_f32_16x16x32_f16 v[4:7], v[56:59], v[156:159], v[4:7]
	v_mul_f32_e32 v244, v242, v244
	v_mfma_f32_16x16x32_f16 v[0:3], v[64:67], v[156:159], v[0:3]
	v_mul_f32_e32 v245, v243, v245
	v_mfma_f32_16x16x32_f16 v[68:71], v[64:67], v[96:99], v[68:71]
	v_max_f32_e32 v242, 0, v188
	s_setprio 0
	s_barrier
	s_mov_b32 m0, s64
	v_lshl_add_u64 v[126:127], v[126:127], 0, s[22:23]
	ds_read_b128 v[44:47], v132
	ds_read_b128 v[56:59], v132 offset:1024
	ds_read_b128 v[60:63], v132 offset:2048
	ds_read_b128 v[64:67], v132 offset:3072
	ds_read_b128 v[80:83], v133
	ds_read_b128 v[96:99], v133 offset:1024
	ds_read_b128 v[136:139], v133 offset:2048
	ds_read_b128 v[140:143], v133 offset:3072
	ds_read_b128 v[144:147], v133 offset:4096
	ds_read_b128 v[148:151], v133 offset:5120
	ds_read_b128 v[152:155], v133 offset:6144
	ds_read_b128 v[156:159], v133 offset:7168
	global_load_lds_dwordx4 v[126:127], off
	v_lshl_add_u64 v[126:127], v[160:161], 0, s[22:23]
	s_mov_b32 m0, s65
	s_add_i32 s46, s76, s54
	global_load_lds_dwordx4 v[126:127], off
	v_lshl_add_u64 v[126:127], v[162:163], 0, s[22:23]
	s_mov_b32 m0, s46
	s_nop 0
	global_load_lds_dwordx4 v[126:127], off
	v_lshl_add_u64 v[126:127], v[164:165], 0, s[22:23]
	s_add_i32 m0, s46, 0x2000
	s_nop 0
	global_load_lds_dwordx4 v[126:127], off
	s_barrier
	s_waitcnt lgkmcnt(0)
	s_setprio 1
	s_waitcnt lgkmcnt(0)
	v_mfma_f32_16x16x32_f16 v[92:95], v[44:47], v[80:83], v[92:95]
	v_max_f32_e32 v243, 0, v189
	v_mfma_f32_16x16x32_f16 v[88:91], v[60:63], v[80:83], v[88:91]
	v_mul_f32_e32 v244, v244, v246
	v_mul_f32_e32 v245, v245, v247
	v_mfma_f32_16x16x32_f16 v[76:79], v[44:47], v[136:139], v[76:79]
	v_fma_f32 v244, -|v188|, v244, v242
	v_mfma_f32_16x16x32_f16 v[72:75], v[60:63], v[136:139], v[72:75]
	v_fma_f32 v245, -|v189|, v245, v243
	v_mfma_f32_16x16x32_f16 v[28:31], v[44:47], v[144:147], v[28:31]
	v_cvt_pk_f16_f32 v186, v244, v245
	v_mfma_f32_16x16x32_f16 v[24:27], v[60:63], v[144:147], v[24:27]
	v_fma_f32 v242, |v190|, s80, 1.0
	v_mfma_f32_16x16x32_f16 v[12:15], v[44:47], v[152:155], v[12:15]
	v_fma_f32 v243, |v191|, s80, 1.0
	v_mfma_f32_16x16x32_f16 v[8:11], v[60:63], v[152:155], v[8:11]
	v_mul_f32_e32 v246, v190, v190
	v_rcp_f32_e32 v242, v242
	v_mfma_f32_16x16x32_f16 v[92:95], v[56:59], v[96:99], v[92:95]
	v_rcp_f32_e32 v243, v243
	v_mfma_f32_16x16x32_f16 v[88:91], v[64:67], v[96:99], v[88:91]
	v_mul_f32_e32 v247, v191, v191
	v_mfma_f32_16x16x32_f16 v[76:79], v[56:59], v[140:143], v[76:79]
	v_mul_f32_e32 v246, s90, v246
	v_mfma_f32_16x16x32_f16 v[72:75], v[64:67], v[140:143], v[72:75]
	v_mul_f32_e32 v247, s90, v247
	v_mfma_f32_16x16x32_f16 v[28:31], v[56:59], v[148:151], v[28:31]
	v_fma_f32 v244, v242, s82, v248
	v_mfma_f32_16x16x32_f16 v[24:27], v[64:67], v[148:151], v[24:27]
	v_fma_f32 v245, v243, s82, v248
	v_exp_f32_e32 v246, v246
	v_mfma_f32_16x16x32_f16 v[12:15], v[56:59], v[156:159], v[12:15]
	v_exp_f32_e32 v247, v247
	v_mfma_f32_16x16x32_f16 v[8:11], v[64:67], v[156:159], v[8:11]
	v_fmaak_f32 v244, v242, v244, 0x3f35f0e3
	s_setprio 0
	s_barrier
	s_add_i32 s46, s48, s54
	v_lshl_add_u64 v[126:127], v[166:167], 0, s[22:23]
	s_mov_b32 m0, s46
	ds_read_b128 v[44:47], v134
	ds_read_b128 v[56:59], v134 offset:1024
	ds_read_b128 v[60:63], v134 offset:2048
	ds_read_b128 v[64:67], v134 offset:3072
	global_load_lds_dwordx4 v[126:127], off
	v_lshl_add_u64 v[126:127], v[168:169], 0, s[22:23]
	s_add_i32 m0, s46, 0x2000
	s_nop 0
	global_load_lds_dwordx4 v[126:127], off
	s_waitcnt vmcnt(6)
	s_barrier
	s_waitcnt lgkmcnt(0)
	s_setprio 1
	s_waitcnt lgkmcnt(0)
	v_mfma_f32_16x16x32_f16 v[84:87], v[44:47], v[80:83], v[84:87]
	v_fmaak_f32 v245, v243, v245, 0x3f35f0e3
	v_mfma_f32_16x16x32_f16 v[68:71], v[60:63], v[80:83], v[68:71]
	v_fmaak_f32 v244, v242, v244, 0xbe11a98e
	v_mfma_f32_16x16x32_f16 v[52:55], v[44:47], v[136:139], v[52:55]
	v_fmaak_f32 v245, v243, v245, 0xbe11a98e
	v_mfma_f32_16x16x32_f16 v[48:51], v[60:63], v[136:139], v[48:51]
	v_fmaak_f32 v244, v242, v244, 0x3e027906
	v_fmaak_f32 v245, v243, v245, 0x3e027906
	v_mfma_f32_16x16x32_f16 v[20:23], v[44:47], v[144:147], v[20:23]
	v_mul_f32_e32 v244, v242, v244
	v_mfma_f32_16x16x32_f16 v[16:19], v[60:63], v[144:147], v[16:19]
	v_mul_f32_e32 v245, v243, v245
	v_mfma_f32_16x16x32_f16 v[4:7], v[44:47], v[152:155], v[4:7]
	v_max_f32_e32 v242, 0, v190
	v_mfma_f32_16x16x32_f16 v[0:3], v[60:63], v[152:155], v[0:3]
	v_max_f32_e32 v243, 0, v191
	v_mfma_f32_16x16x32_f16 v[84:87], v[56:59], v[96:99], v[84:87]
	v_mul_f32_e32 v244, v244, v246
	v_mfma_f32_16x16x32_f16 v[80:83], v[64:67], v[96:99], v[68:71]
	v_mul_f32_e32 v245, v245, v247
	v_fma_f32 v244, -|v190|, v244, v242
	v_mfma_f32_16x16x32_f16 v[52:55], v[56:59], v[140:143], v[52:55]
	v_fma_f32 v245, -|v191|, v245, v243
	v_mfma_f32_16x16x32_f16 v[48:51], v[64:67], v[140:143], v[48:51]
	v_cvt_pk_f16_f32 v187, v244, v245
	v_mfma_f32_16x16x32_f16 v[20:23], v[56:59], v[148:151], v[20:23]
	global_store_dwordx4 v[250:251], v[184:187], off offset:256 sc1
	v_mfma_f32_16x16x32_f16 v[16:19], v[64:67], v[148:151], v[16:19]
	v_fma_f32 v242, |v200|, s80, 1.0
	v_mfma_f32_16x16x32_f16 v[4:7], v[56:59], v[156:159], v[4:7]
	v_fma_f32 v243, |v201|, s80, 1.0
	v_mfma_f32_16x16x32_f16 v[0:3], v[64:67], v[156:159], v[0:3]
	v_mul_f32_e32 v246, v200, v200
	v_rcp_f32_e32 v242, v242
	s_setprio 0
	s_barrier
	s_add_i32 s75, s75, 3
	s_add_u32 s44, s44, 0x180
	s_addc_u32 s45, s45, 0
	s_add_u32 s46, s40, s44
	s_addc_u32 s47, s41, s45
	s_add_u32 s46, s46, 0x180
	s_addc_u32 s47, s47, 0
	s_add_u32 s48, s42, s44
	s_addc_u32 s49, s43, s45
	s_add_u32 s76, s48, 0x180
	s_addc_u32 s77, s49, 0
	s_cmp_eq_u32 s67, s75
	s_cselect_b32 s49, s7, s47
	s_cselect_b32 s48, s6, s46
	s_cselect_b32 s47, s5, s77
	s_cselect_b32 s46, s4, s76
	s_add_i32 s76, s19, s54
	v_lshl_add_u64 v[126:127], v[32:33], 0, s[44:45]
	s_mov_b32 m0, s76
	ds_read_b128 v[44:47], v130 offset:16384
	ds_read_b128 v[56:59], v130 offset:17408
	ds_read_b128 v[60:63], v130 offset:18432
	ds_read_b128 v[64:67], v130 offset:19456
	ds_read_b128 v[68:71], v131
	ds_read_b128 v[96:99], v131 offset:1024
	ds_read_b128 v[136:139], v131 offset:2048
	ds_read_b128 v[140:143], v131 offset:3072
	ds_read_b128 v[144:147], v131 offset:4096
	ds_read_b128 v[148:151], v131 offset:5120
	ds_read_b128 v[152:155], v131 offset:6144
	ds_read_b128 v[156:159], v131 offset:7168
	global_load_lds_dwordx4 v[126:127], off
	v_lshl_add_u64 v[126:127], v[34:35], 0, s[44:45]
	s_add_i32 m0, s76, 0x2000
	s_add_i32 s76, s27, s54
	global_load_lds_dwordx4 v[126:127], off
	v_lshl_add_u64 v[126:127], v[36:37], 0, s[44:45]
	s_mov_b32 m0, s76
	s_nop 0
	global_load_lds_dwordx4 v[126:127], off
	v_lshl_add_u64 v[126:127], v[38:39], 0, s[44:45]
	s_add_i32 m0, s76, 0x2000
	s_nop 0
	global_load_lds_dwordx4 v[126:127], off
	s_barrier
	s_waitcnt lgkmcnt(0)
	s_setprio 1
	s_waitcnt lgkmcnt(0)
	v_mfma_f32_16x16x32_f16 v[92:95], v[44:47], v[68:71], v[92:95]
	v_rcp_f32_e32 v243, v243
	v_mfma_f32_16x16x32_f16 v[88:91], v[60:63], v[68:71], v[88:91]
	v_mul_f32_e32 v247, v201, v201
	v_mfma_f32_16x16x32_f16 v[76:79], v[44:47], v[136:139], v[76:79]
	v_mul_f32_e32 v246, s90, v246
	v_mfma_f32_16x16x32_f16 v[72:75], v[60:63], v[136:139], v[72:75]
	v_mul_f32_e32 v247, s90, v247
	v_mfma_f32_16x16x32_f16 v[28:31], v[44:47], v[144:147], v[28:31]
	v_fma_f32 v244, v242, s82, v248
	v_mfma_f32_16x16x32_f16 v[24:27], v[60:63], v[144:147], v[24:27]
	v_fma_f32 v245, v243, s82, v248
	v_exp_f32_e32 v246, v246
	v_mfma_f32_16x16x32_f16 v[12:15], v[44:47], v[152:155], v[12:15]
	v_exp_f32_e32 v247, v247
	v_mfma_f32_16x16x32_f16 v[8:11], v[60:63], v[152:155], v[8:11]
	v_fmaak_f32 v244, v242, v244, 0x3f35f0e3
	v_mfma_f32_16x16x32_f16 v[92:95], v[56:59], v[96:99], v[92:95]
	v_fmaak_f32 v245, v243, v245, 0x3f35f0e3
	v_mfma_f32_16x16x32_f16 v[88:91], v[64:67], v[96:99], v[88:91]
	v_fmaak_f32 v244, v242, v244, 0xbe11a98e
	v_mfma_f32_16x16x32_f16 v[76:79], v[56:59], v[140:143], v[76:79]
	v_fmaak_f32 v245, v243, v245, 0xbe11a98e
	v_mfma_f32_16x16x32_f16 v[72:75], v[64:67], v[140:143], v[72:75]
	v_fmaak_f32 v244, v242, v244, 0x3e027906
	v_fmaak_f32 v245, v243, v245, 0x3e027906
	v_mfma_f32_16x16x32_f16 v[28:31], v[56:59], v[148:151], v[28:31]
	v_mul_f32_e32 v244, v242, v244
	v_mfma_f32_16x16x32_f16 v[24:27], v[64:67], v[148:151], v[24:27]
	v_mul_f32_e32 v245, v243, v245
	v_mfma_f32_16x16x32_f16 v[12:15], v[56:59], v[156:159], v[12:15]
	v_max_f32_e32 v242, 0, v200
	v_mfma_f32_16x16x32_f16 v[8:11], v[64:67], v[156:159], v[8:11]
	v_max_f32_e32 v243, 0, v201
	s_setprio 0
	s_barrier
	s_add_i32 s76, s68, s54
	v_lshl_add_u64 v[126:127], v[40:41], 0, s[44:45]
	s_mov_b32 m0, s76
	ds_read_b128 v[44:47], v130 offset:32768
	ds_read_b128 v[56:59], v130 offset:33792
	ds_read_b128 v[60:63], v130 offset:34816
	ds_read_b128 v[64:67], v130 offset:35840
	global_load_lds_dwordx4 v[126:127], off
	v_lshl_add_u64 v[126:127], v[42:43], 0, s[44:45]
	s_add_i32 m0, s76, 0x2000
	s_nop 0
	global_load_lds_dwordx4 v[126:127], off
	s_waitcnt vmcnt(7)
	s_barrier
	s_waitcnt lgkmcnt(0)
	s_setprio 1
	s_waitcnt lgkmcnt(0)
	v_mfma_f32_16x16x32_f16 v[84:87], v[44:47], v[68:71], v[84:87]
	v_mul_f32_e32 v244, v244, v246
	v_mfma_f32_16x16x32_f16 v[52:55], v[44:47], v[136:139], v[52:55]
	v_mul_f32_e32 v245, v245, v247
	v_fma_f32 v244, -|v200|, v244, v242
	v_mfma_f32_16x16x32_f16 v[48:51], v[60:63], v[136:139], v[48:51]
	v_fma_f32 v245, -|v201|, v245, v243
	v_mfma_f32_16x16x32_f16 v[20:23], v[44:47], v[144:147], v[20:23]
	v_cvt_pk_f16_f32 v200, v244, v245
	v_mfma_f32_16x16x32_f16 v[16:19], v[60:63], v[144:147], v[16:19]
	v_fma_f32 v242, |v202|, s80, 1.0
	v_mfma_f32_16x16x32_f16 v[4:7], v[44:47], v[152:155], v[4:7]
	v_fma_f32 v243, |v203|, s80, 1.0
	v_mfma_f32_16x16x32_f16 v[0:3], v[60:63], v[152:155], v[0:3]
	v_mul_f32_e32 v246, v202, v202
	v_mfma_f32_16x16x32_f16 v[84:87], v[56:59], v[96:99], v[84:87]
	v_rcp_f32_e32 v242, v242
	v_rcp_f32_e32 v243, v243
	v_mfma_f32_16x16x32_f16 v[68:71], v[60:63], v[68:71], v[80:83]
	v_mul_f32_e32 v247, v203, v203
	v_mfma_f32_16x16x32_f16 v[52:55], v[56:59], v[140:143], v[52:55]
	v_mul_f32_e32 v246, s90, v246
	v_mfma_f32_16x16x32_f16 v[48:51], v[64:67], v[140:143], v[48:51]
	v_mul_f32_e32 v247, s90, v247
	v_mfma_f32_16x16x32_f16 v[20:23], v[56:59], v[148:151], v[20:23]
	v_fma_f32 v244, v242, s82, v248
	v_mfma_f32_16x16x32_f16 v[16:19], v[64:67], v[148:151], v[16:19]
	v_fma_f32 v245, v243, s82, v248
	v_mfma_f32_16x16x32_f16 v[4:7], v[56:59], v[156:159], v[4:7]
	v_exp_f32_e32 v246, v246
	v_exp_f32_e32 v247, v247
	v_mfma_f32_16x16x32_f16 v[0:3], v[64:67], v[156:159], v[0:3]
	v_fmaak_f32 v244, v242, v244, 0x3f35f0e3
	v_mfma_f32_16x16x32_f16 v[68:71], v[64:67], v[96:99], v[68:71]
	v_fmaak_f32 v245, v243, v245, 0x3f35f0e3
	s_setprio 0
	s_barrier
	s_add_i32 s76, 0, 0x10000
	s_mov_b32 m0, s57
	v_add_u32_e32 v64, s76, v128
	v_lshl_add_u64 v[126:127], s[48:49], 0, v[100:101]
	ds_read_b128 v[44:47], v64
	ds_read_b128 v[56:59], v64 offset:1024
	ds_read_b128 v[60:63], v64 offset:2048
	ds_read_b128 v[64:67], v64 offset:3072
	ds_read_b128 v[80:83], v131 offset:49152
	ds_read_b128 v[96:99], v131 offset:50176
	ds_read_b128 v[136:139], v131 offset:51200
	ds_read_b128 v[140:143], v131 offset:52224
	ds_read_b128 v[144:147], v131 offset:53248
	ds_read_b128 v[148:151], v131 offset:54272
	ds_read_b128 v[152:155], v131 offset:55296
	ds_read_b128 v[156:159], v131 offset:56320
	global_load_lds_dwordx4 v[126:127], off
	v_lshl_add_u64 v[160:161], s[48:49], 0, v[104:105]
	s_mov_b32 m0, s58
	v_lshl_add_u64 v[162:163], s[46:47], 0, v[102:103]
	global_load_lds_dwordx4 v[160:161], off
	s_mov_b32 m0, s59
	v_lshl_add_u64 v[164:165], s[46:47], 0, v[106:107]
	global_load_lds_dwordx4 v[162:163], off
	s_mov_b32 m0, s60
	s_nop 0
	global_load_lds_dwordx4 v[164:165], off
	s_barrier
	s_waitcnt lgkmcnt(0)
	s_setprio 1
	s_waitcnt lgkmcnt(0)
	v_mfma_f32_16x16x32_f16 v[92:95], v[44:47], v[80:83], v[92:95]
	v_fmaak_f32 v244, v242, v244, 0xbe11a98e
	v_mfma_f32_16x16x32_f16 v[88:91], v[60:63], v[80:83], v[88:91]
	v_fmaak_f32 v245, v243, v245, 0xbe11a98e
	v_mfma_f32_16x16x32_f16 v[76:79], v[44:47], v[136:139], v[76:79]
	v_fmaak_f32 v244, v242, v244, 0x3e027906
	v_mfma_f32_16x16x32_f16 v[72:75], v[60:63], v[136:139], v[72:75]
	v_fmaak_f32 v245, v243, v245, 0x3e027906
	v_mul_f32_e32 v244, v242, v244
	v_mfma_f32_16x16x32_f16 v[28:31], v[44:47], v[144:147], v[28:31]
	v_mul_f32_e32 v245, v243, v245
	v_mfma_f32_16x16x32_f16 v[24:27], v[60:63], v[144:147], v[24:27]
	v_max_f32_e32 v242, 0, v202
	v_mfma_f32_16x16x32_f16 v[12:15], v[44:47], v[152:155], v[12:15]
	v_max_f32_e32 v243, 0, v203
	v_mfma_f32_16x16x32_f16 v[8:11], v[60:63], v[152:155], v[8:11]
	v_mul_f32_e32 v244, v244, v246
	v_mfma_f32_16x16x32_f16 v[92:95], v[56:59], v[96:99], v[92:95]
	v_mul_f32_e32 v245, v245, v247
	v_mfma_f32_16x16x32_f16 v[88:91], v[64:67], v[96:99], v[88:91]
	v_fma_f32 v244, -|v202|, v244, v242
	v_fma_f32 v245, -|v203|, v245, v243
	v_mfma_f32_16x16x32_f16 v[76:79], v[56:59], v[140:143], v[76:79]
	v_cvt_pk_f16_f32 v201, v244, v245
	v_mfma_f32_16x16x32_f16 v[72:75], v[64:67], v[140:143], v[72:75]
	v_fma_f32 v242, |v204|, s80, 1.0
	v_mfma_f32_16x16x32_f16 v[28:31], v[56:59], v[148:151], v[28:31]
	v_fma_f32 v243, |v205|, s80, 1.0
	v_mfma_f32_16x16x32_f16 v[24:27], v[64:67], v[148:151], v[24:27]
	v_mul_f32_e32 v246, v204, v204
	v_mfma_f32_16x16x32_f16 v[12:15], v[56:59], v[156:159], v[12:15]
	v_rcp_f32_e32 v242, v242
	v_mfma_f32_16x16x32_f16 v[8:11], v[64:67], v[156:159], v[8:11]
	v_rcp_f32_e32 v243, v243
	v_mul_f32_e32 v247, v205, v205
	s_setprio 0
	s_barrier
	s_add_i32 s48, 0, 0x14000
	s_add_u32 s46, s46, s10
	s_addc_u32 s47, s47, s11
	s_mov_b32 m0, s61
	v_add_u32_e32 v64, s48, v128
	v_lshl_add_u64 v[166:167], s[46:47], 0, v[102:103]
	ds_read_b128 v[44:47], v64
	ds_read_b128 v[56:59], v64 offset:1024
	ds_read_b128 v[60:63], v64 offset:2048
	ds_read_b128 v[64:67], v64 offset:3072
	global_load_lds_dwordx4 v[166:167], off
	v_lshl_add_u64 v[168:169], s[46:47], 0, v[106:107]
	s_mov_b32 m0, s62
	s_nop 0
	global_load_lds_dwordx4 v[168:169], off
	s_waitcnt vmcnt(6)
	s_barrier
	s_waitcnt lgkmcnt(0)
	s_setprio 1
	s_waitcnt lgkmcnt(0)
	v_mfma_f32_16x16x32_f16 v[84:87], v[44:47], v[80:83], v[84:87]
	v_mul_f32_e32 v246, s90, v246
	v_mfma_f32_16x16x32_f16 v[52:55], v[44:47], v[136:139], v[52:55]
	v_mul_f32_e32 v247, s90, v247
	v_mfma_f32_16x16x32_f16 v[48:51], v[60:63], v[136:139], v[48:51]
	v_fma_f32 v244, v242, s82, v248
	v_mfma_f32_16x16x32_f16 v[20:23], v[44:47], v[144:147], v[20:23]
	v_fma_f32 v245, v243, s82, v248
	v_mfma_f32_16x16x32_f16 v[16:19], v[60:63], v[144:147], v[16:19]
	v_exp_f32_e32 v246, v246
	v_mfma_f32_16x16x32_f16 v[4:7], v[44:47], v[152:155], v[4:7]
	v_exp_f32_e32 v247, v247
	v_fmaak_f32 v244, v242, v244, 0x3f35f0e3
	v_mfma_f32_16x16x32_f16 v[0:3], v[60:63], v[152:155], v[0:3]
	v_fmaak_f32 v245, v243, v245, 0x3f35f0e3
	v_mfma_f32_16x16x32_f16 v[84:87], v[56:59], v[96:99], v[84:87]
	v_fmaak_f32 v244, v242, v244, 0xbe11a98e
	v_mfma_f32_16x16x32_f16 v[68:71], v[60:63], v[80:83], v[68:71]
	v_fmaak_f32 v245, v243, v245, 0xbe11a98e
	v_mfma_f32_16x16x32_f16 v[52:55], v[56:59], v[140:143], v[52:55]
	v_fmaak_f32 v244, v242, v244, 0x3e027906
	v_mfma_f32_16x16x32_f16 v[48:51], v[64:67], v[140:143], v[48:51]
	v_fmaak_f32 v245, v243, v245, 0x3e027906
	v_mfma_f32_16x16x32_f16 v[20:23], v[56:59], v[148:151], v[20:23]
	v_mul_f32_e32 v244, v242, v244
	v_mul_f32_e32 v245, v243, v245
	v_mfma_f32_16x16x32_f16 v[16:19], v[64:67], v[148:151], v[16:19]
	v_max_f32_e32 v242, 0, v204
	v_mfma_f32_16x16x32_f16 v[4:7], v[56:59], v[156:159], v[4:7]
	v_max_f32_e32 v243, 0, v205
	v_mfma_f32_16x16x32_f16 v[0:3], v[64:67], v[156:159], v[0:3]
	v_mul_f32_e32 v244, v244, v246
	v_mfma_f32_16x16x32_f16 v[68:71], v[64:67], v[96:99], v[68:71]
	v_mul_f32_e32 v245, v245, v247
	s_setprio 0
	s_barrier
	s_mov_b32 m0, s64
	v_lshl_add_u64 v[126:127], v[126:127], 0, s[22:23]
	ds_read_b128 v[44:47], v132
	ds_read_b128 v[56:59], v132 offset:1024
	ds_read_b128 v[60:63], v132 offset:2048
	ds_read_b128 v[64:67], v132 offset:3072
	ds_read_b128 v[80:83], v133
	ds_read_b128 v[96:99], v133 offset:1024
	ds_read_b128 v[136:139], v133 offset:2048
	ds_read_b128 v[140:143], v133 offset:3072
	ds_read_b128 v[144:147], v133 offset:4096
	ds_read_b128 v[148:151], v133 offset:5120
	ds_read_b128 v[152:155], v133 offset:6144
	ds_read_b128 v[156:159], v133 offset:7168
	global_load_lds_dwordx4 v[126:127], off
	v_lshl_add_u64 v[126:127], v[160:161], 0, s[22:23]
	s_mov_b32 m0, s65
	s_add_i32 s46, s76, s54
	global_load_lds_dwordx4 v[126:127], off
	v_lshl_add_u64 v[126:127], v[162:163], 0, s[22:23]
	s_mov_b32 m0, s46
	s_nop 0
	global_load_lds_dwordx4 v[126:127], off
	v_lshl_add_u64 v[126:127], v[164:165], 0, s[22:23]
	s_add_i32 m0, s46, 0x2000
	s_nop 0
	global_load_lds_dwordx4 v[126:127], off
	s_barrier
	s_waitcnt lgkmcnt(0)
	s_setprio 1
	s_waitcnt lgkmcnt(0)
	v_mfma_f32_16x16x32_f16 v[92:95], v[44:47], v[80:83], v[92:95]
	v_fma_f32 v244, -|v204|, v244, v242
	v_mfma_f32_16x16x32_f16 v[88:91], v[60:63], v[80:83], v[88:91]
	v_fma_f32 v245, -|v205|, v245, v243
	v_cvt_pk_f16_f32 v202, v244, v245
	v_mfma_f32_16x16x32_f16 v[76:79], v[44:47], v[136:139], v[76:79]
	v_fma_f32 v242, |v206|, s80, 1.0
	v_mfma_f32_16x16x32_f16 v[72:75], v[60:63], v[136:139], v[72:75]
	v_fma_f32 v243, |v207|, s80, 1.0
	v_mfma_f32_16x16x32_f16 v[28:31], v[44:47], v[144:147], v[28:31]
	v_mul_f32_e32 v246, v206, v206
	v_mfma_f32_16x16x32_f16 v[24:27], v[60:63], v[144:147], v[24:27]
	v_rcp_f32_e32 v242, v242
	v_mfma_f32_16x16x32_f16 v[12:15], v[44:47], v[152:155], v[12:15]
	v_rcp_f32_e32 v243, v243
	v_mfma_f32_16x16x32_f16 v[8:11], v[60:63], v[152:155], v[8:11]
	v_mul_f32_e32 v247, v207, v207
	v_mul_f32_e32 v246, s90, v246
	v_mfma_f32_16x16x32_f16 v[92:95], v[56:59], v[96:99], v[92:95]
	v_mul_f32_e32 v247, s90, v247
	v_mfma_f32_16x16x32_f16 v[88:91], v[64:67], v[96:99], v[88:91]
	v_fma_f32 v244, v242, s82, v248
	v_mfma_f32_16x16x32_f16 v[76:79], v[56:59], v[140:143], v[76:79]
	v_fma_f32 v245, v243, s82, v248
	v_mfma_f32_16x16x32_f16 v[72:75], v[64:67], v[140:143], v[72:75]
	v_exp_f32_e32 v246, v246
	v_mfma_f32_16x16x32_f16 v[28:31], v[56:59], v[148:151], v[28:31]
	v_exp_f32_e32 v247, v247
	v_mfma_f32_16x16x32_f16 v[24:27], v[64:67], v[148:151], v[24:27]
	v_fmaak_f32 v244, v242, v244, 0x3f35f0e3
	v_fmaak_f32 v245, v243, v245, 0x3f35f0e3
	v_mfma_f32_16x16x32_f16 v[12:15], v[56:59], v[156:159], v[12:15]
	v_fmaak_f32 v244, v242, v244, 0xbe11a98e
	v_mfma_f32_16x16x32_f16 v[8:11], v[64:67], v[156:159], v[8:11]
	v_fmaak_f32 v245, v243, v245, 0xbe11a98e
	s_setprio 0
	s_barrier
	s_add_i32 s46, s48, s54
	v_lshl_add_u64 v[126:127], v[166:167], 0, s[22:23]
	s_mov_b32 m0, s46
	ds_read_b128 v[44:47], v134
	ds_read_b128 v[56:59], v134 offset:1024
	ds_read_b128 v[60:63], v134 offset:2048
	ds_read_b128 v[64:67], v134 offset:3072
	global_load_lds_dwordx4 v[126:127], off
	v_lshl_add_u64 v[126:127], v[168:169], 0, s[22:23]
	s_add_i32 m0, s46, 0x2000
	s_nop 0
	global_load_lds_dwordx4 v[126:127], off
	s_waitcnt vmcnt(6)
	s_barrier
	s_waitcnt lgkmcnt(0)
	s_setprio 1
	s_waitcnt lgkmcnt(0)
	v_mfma_f32_16x16x32_f16 v[84:87], v[44:47], v[80:83], v[84:87]
	v_fmaak_f32 v244, v242, v244, 0x3e027906
	v_mfma_f32_16x16x32_f16 v[68:71], v[60:63], v[80:83], v[68:71]
	v_fmaak_f32 v245, v243, v245, 0x3e027906
	v_mfma_f32_16x16x32_f16 v[52:55], v[44:47], v[136:139], v[52:55]
	v_mul_f32_e32 v244, v242, v244
	v_mfma_f32_16x16x32_f16 v[48:51], v[60:63], v[136:139], v[48:51]
	v_mul_f32_e32 v245, v243, v245
	v_max_f32_e32 v242, 0, v206
	v_mfma_f32_16x16x32_f16 v[20:23], v[44:47], v[144:147], v[20:23]
	v_max_f32_e32 v243, 0, v207
	v_mfma_f32_16x16x32_f16 v[16:19], v[60:63], v[144:147], v[16:19]
	v_mul_f32_e32 v244, v244, v246
	v_mfma_f32_16x16x32_f16 v[4:7], v[44:47], v[152:155], v[4:7]
	v_mul_f32_e32 v245, v245, v247
	v_mfma_f32_16x16x32_f16 v[0:3], v[60:63], v[152:155], v[0:3]
	v_fma_f32 v244, -|v206|, v244, v242
	v_mfma_f32_16x16x32_f16 v[84:87], v[56:59], v[96:99], v[84:87]
	v_fma_f32 v245, -|v207|, v245, v243
	v_mfma_f32_16x16x32_f16 v[80:83], v[64:67], v[96:99], v[68:71]
	v_cvt_pk_f16_f32 v203, v244, v245
	v_lshl_add_u64 v[252:253], v[250:251], 0, s[92:93]
	v_mfma_f32_16x16x32_f16 v[52:55], v[56:59], v[140:143], v[52:55]
	global_store_dwordx4 v[252:253], v[200:203], off offset:256 sc1
	v_mfma_f32_16x16x32_f16 v[48:51], v[64:67], v[140:143], v[48:51]
	v_fma_f32 v242, |v216|, s80, 1.0
	v_mfma_f32_16x16x32_f16 v[20:23], v[56:59], v[148:151], v[20:23]
	v_fma_f32 v243, |v217|, s80, 1.0
	v_mfma_f32_16x16x32_f16 v[16:19], v[64:67], v[148:151], v[16:19]
	v_mul_f32_e32 v246, v216, v216
	v_mfma_f32_16x16x32_f16 v[4:7], v[56:59], v[156:159], v[4:7]
	v_rcp_f32_e32 v242, v242
	v_rcp_f32_e32 v243, v243
	v_mfma_f32_16x16x32_f16 v[0:3], v[64:67], v[156:159], v[0:3]
	v_mul_f32_e32 v247, v217, v217
	s_setprio 0
	s_barrier
	s_add_i32 s75, s75, 3
	s_add_u32 s44, s44, 0x180
	s_addc_u32 s45, s45, 0
	s_add_u32 s46, s40, s44
	s_addc_u32 s47, s41, s45
	s_add_u32 s46, s46, 0x180
	s_addc_u32 s47, s47, 0
	s_add_u32 s48, s42, s44
	s_addc_u32 s49, s43, s45
	s_add_u32 s76, s48, 0x180
	s_addc_u32 s77, s49, 0
	s_cmp_eq_u32 s67, s75
	s_cselect_b32 s49, s7, s47
	s_cselect_b32 s48, s6, s46
	s_cselect_b32 s47, s5, s77
	s_cselect_b32 s46, s4, s76
	s_add_i32 s76, s19, s54
	v_lshl_add_u64 v[126:127], v[32:33], 0, s[44:45]
	s_mov_b32 m0, s76
	ds_read_b128 v[44:47], v130 offset:16384
	ds_read_b128 v[56:59], v130 offset:17408
	ds_read_b128 v[60:63], v130 offset:18432
	ds_read_b128 v[64:67], v130 offset:19456
	ds_read_b128 v[68:71], v131
	ds_read_b128 v[96:99], v131 offset:1024
	ds_read_b128 v[136:139], v131 offset:2048
	ds_read_b128 v[140:143], v131 offset:3072
	ds_read_b128 v[144:147], v131 offset:4096
	ds_read_b128 v[148:151], v131 offset:5120
	ds_read_b128 v[152:155], v131 offset:6144
	ds_read_b128 v[156:159], v131 offset:7168
	global_load_lds_dwordx4 v[126:127], off
	v_lshl_add_u64 v[126:127], v[34:35], 0, s[44:45]
	s_add_i32 m0, s76, 0x2000
	s_add_i32 s76, s27, s54
	global_load_lds_dwordx4 v[126:127], off
	v_lshl_add_u64 v[126:127], v[36:37], 0, s[44:45]
	s_mov_b32 m0, s76
	s_nop 0
	global_load_lds_dwordx4 v[126:127], off
	v_lshl_add_u64 v[126:127], v[38:39], 0, s[44:45]
	s_add_i32 m0, s76, 0x2000
	s_nop 0
	global_load_lds_dwordx4 v[126:127], off
	s_barrier
	s_waitcnt lgkmcnt(0)
	s_setprio 1
	s_waitcnt lgkmcnt(0)
	v_mfma_f32_16x16x32_f16 v[92:95], v[44:47], v[68:71], v[92:95]
	v_mul_f32_e32 v246, s90, v246
	v_mfma_f32_16x16x32_f16 v[88:91], v[60:63], v[68:71], v[88:91]
	v_mul_f32_e32 v247, s90, v247
	v_mfma_f32_16x16x32_f16 v[76:79], v[44:47], v[136:139], v[76:79]
	v_fma_f32 v244, v242, s82, v248
	v_mfma_f32_16x16x32_f16 v[72:75], v[60:63], v[136:139], v[72:75]
	v_fma_f32 v245, v243, s82, v248
	v_mfma_f32_16x16x32_f16 v[28:31], v[44:47], v[144:147], v[28:31]
	v_exp_f32_e32 v246, v246
	v_exp_f32_e32 v247, v247
	v_mfma_f32_16x16x32_f16 v[24:27], v[60:63], v[144:147], v[24:27]
	v_fmaak_f32 v244, v242, v244, 0x3f35f0e3
	v_mfma_f32_16x16x32_f16 v[12:15], v[44:47], v[152:155], v[12:15]
	v_fmaak_f32 v245, v243, v245, 0x3f35f0e3
	v_mfma_f32_16x16x32_f16 v[8:11], v[60:63], v[152:155], v[8:11]
	v_fmaak_f32 v244, v242, v244, 0xbe11a98e
	v_mfma_f32_16x16x32_f16 v[92:95], v[56:59], v[96:99], v[92:95]
	v_fmaak_f32 v245, v243, v245, 0xbe11a98e
	v_mfma_f32_16x16x32_f16 v[88:91], v[64:67], v[96:99], v[88:91]
	v_fmaak_f32 v244, v242, v244, 0x3e027906
	v_mfma_f32_16x16x32_f16 v[76:79], v[56:59], v[140:143], v[76:79]
	v_fmaak_f32 v245, v243, v245, 0x3e027906
	v_mul_f32_e32 v244, v242, v244
	v_mfma_f32_16x16x32_f16 v[72:75], v[64:67], v[140:143], v[72:75]
	v_mul_f32_e32 v245, v243, v245
	v_mfma_f32_16x16x32_f16 v[28:31], v[56:59], v[148:151], v[28:31]
	v_max_f32_e32 v242, 0, v216
	v_mfma_f32_16x16x32_f16 v[24:27], v[64:67], v[148:151], v[24:27]
	v_max_f32_e32 v243, 0, v217
	v_mfma_f32_16x16x32_f16 v[12:15], v[56:59], v[156:159], v[12:15]
	v_mul_f32_e32 v244, v244, v246
	v_mfma_f32_16x16x32_f16 v[8:11], v[64:67], v[156:159], v[8:11]
	v_mul_f32_e32 v245, v245, v247
	s_setprio 0
	s_barrier
	s_add_i32 s76, s68, s54
	v_lshl_add_u64 v[126:127], v[40:41], 0, s[44:45]
	s_mov_b32 m0, s76
	ds_read_b128 v[44:47], v130 offset:32768
	ds_read_b128 v[56:59], v130 offset:33792
	ds_read_b128 v[60:63], v130 offset:34816
	ds_read_b128 v[64:67], v130 offset:35840
	global_load_lds_dwordx4 v[126:127], off
	v_lshl_add_u64 v[126:127], v[42:43], 0, s[44:45]
	s_add_i32 m0, s76, 0x2000
	s_nop 0
	global_load_lds_dwordx4 v[126:127], off
	s_waitcnt vmcnt(7)
	s_barrier
	s_waitcnt lgkmcnt(0)
	s_setprio 1
	s_waitcnt lgkmcnt(0)
	v_mfma_f32_16x16x32_f16 v[84:87], v[44:47], v[68:71], v[84:87]
	v_fma_f32 v244, -|v216|, v244, v242
	v_fma_f32 v245, -|v217|, v245, v243
	v_mfma_f32_16x16x32_f16 v[52:55], v[44:47], v[136:139], v[52:55]
	v_cvt_pk_f16_f32 v216, v244, v245
	v_mfma_f32_16x16x32_f16 v[48:51], v[60:63], v[136:139], v[48:51]
	v_fma_f32 v242, |v218|, s80, 1.0
	v_mfma_f32_16x16x32_f16 v[20:23], v[44:47], v[144:147], v[20:23]
	v_fma_f32 v243, |v219|, s80, 1.0
	v_mfma_f32_16x16x32_f16 v[16:19], v[60:63], v[144:147], v[16:19]
	v_mul_f32_e32 v246, v218, v218
	v_mfma_f32_16x16x32_f16 v[4:7], v[44:47], v[152:155], v[4:7]
	v_rcp_f32_e32 v242, v242
	v_mfma_f32_16x16x32_f16 v[0:3], v[60:63], v[152:155], v[0:3]
	v_rcp_f32_e32 v243, v243
	v_mul_f32_e32 v247, v219, v219
	v_mfma_f32_16x16x32_f16 v[84:87], v[56:59], v[96:99], v[84:87]
	v_mul_f32_e32 v246, s90, v246
	v_mfma_f32_16x16x32_f16 v[68:71], v[60:63], v[68:71], v[80:83]
	v_mul_f32_e32 v247, s90, v247
	v_mfma_f32_16x16x32_f16 v[52:55], v[56:59], v[140:143], v[52:55]
	v_fma_f32 v244, v242, s82, v248
	v_mfma_f32_16x16x32_f16 v[48:51], v[64:67], v[140:143], v[48:51]
	v_fma_f32 v245, v243, s82, v248
	v_mfma_f32_16x16x32_f16 v[20:23], v[56:59], v[148:151], v[20:23]
	v_exp_f32_e32 v246, v246
	v_mfma_f32_16x16x32_f16 v[16:19], v[64:67], v[148:151], v[16:19]
	v_exp_f32_e32 v247, v247
	v_fmaak_f32 v244, v242, v244, 0x3f35f0e3
	v_mfma_f32_16x16x32_f16 v[4:7], v[56:59], v[156:159], v[4:7]
	v_fmaak_f32 v245, v243, v245, 0x3f35f0e3
	v_mfma_f32_16x16x32_f16 v[0:3], v[64:67], v[156:159], v[0:3]
	v_fmaak_f32 v244, v242, v244, 0xbe11a98e
	v_mfma_f32_16x16x32_f16 v[68:71], v[64:67], v[96:99], v[68:71]
	v_fmaak_f32 v245, v243, v245, 0xbe11a98e
	s_setprio 0
	s_barrier
	s_add_i32 s76, 0, 0x10000
	s_mov_b32 m0, s57
	v_add_u32_e32 v64, s76, v128
	v_lshl_add_u64 v[126:127], s[48:49], 0, v[100:101]
	ds_read_b128 v[44:47], v64
	ds_read_b128 v[56:59], v64 offset:1024
	ds_read_b128 v[60:63], v64 offset:2048
	ds_read_b128 v[64:67], v64 offset:3072
	ds_read_b128 v[80:83], v131 offset:49152
	ds_read_b128 v[96:99], v131 offset:50176
	ds_read_b128 v[136:139], v131 offset:51200
	ds_read_b128 v[140:143], v131 offset:52224
	ds_read_b128 v[144:147], v131 offset:53248
	ds_read_b128 v[148:151], v131 offset:54272
	ds_read_b128 v[152:155], v131 offset:55296
	ds_read_b128 v[156:159], v131 offset:56320
	global_load_lds_dwordx4 v[126:127], off
	v_lshl_add_u64 v[160:161], s[48:49], 0, v[104:105]
	s_mov_b32 m0, s58
	v_lshl_add_u64 v[162:163], s[46:47], 0, v[102:103]
	global_load_lds_dwordx4 v[160:161], off
	s_mov_b32 m0, s59
	v_lshl_add_u64 v[164:165], s[46:47], 0, v[106:107]
	global_load_lds_dwordx4 v[162:163], off
	s_mov_b32 m0, s60
	s_nop 0
	global_load_lds_dwordx4 v[164:165], off
	s_barrier
	s_waitcnt lgkmcnt(0)
	s_setprio 1
	s_waitcnt lgkmcnt(0)
	v_mfma_f32_16x16x32_f16 v[92:95], v[44:47], v[80:83], v[92:95]
	v_fmaak_f32 v244, v242, v244, 0x3e027906
	v_mfma_f32_16x16x32_f16 v[88:91], v[60:63], v[80:83], v[88:91]
	v_fmaak_f32 v245, v243, v245, 0x3e027906
	v_mfma_f32_16x16x32_f16 v[76:79], v[44:47], v[136:139], v[76:79]
	v_mul_f32_e32 v244, v242, v244
	v_mul_f32_e32 v245, v243, v245
	v_mfma_f32_16x16x32_f16 v[72:75], v[60:63], v[136:139], v[72:75]
	v_max_f32_e32 v242, 0, v218
	v_mfma_f32_16x16x32_f16 v[28:31], v[44:47], v[144:147], v[28:31]
	v_max_f32_e32 v243, 0, v219
	v_mfma_f32_16x16x32_f16 v[24:27], v[60:63], v[144:147], v[24:27]
	v_mul_f32_e32 v244, v244, v246
	v_mfma_f32_16x16x32_f16 v[12:15], v[44:47], v[152:155], v[12:15]
	v_mul_f32_e32 v245, v245, v247
	v_mfma_f32_16x16x32_f16 v[8:11], v[60:63], v[152:155], v[8:11]
	v_fma_f32 v244, -|v218|, v244, v242
	v_mfma_f32_16x16x32_f16 v[92:95], v[56:59], v[96:99], v[92:95]
	v_fma_f32 v245, -|v219|, v245, v243
	v_cvt_pk_f16_f32 v217, v244, v245
	v_mfma_f32_16x16x32_f16 v[88:91], v[64:67], v[96:99], v[88:91]
	v_fma_f32 v242, |v220|, s80, 1.0
	v_mfma_f32_16x16x32_f16 v[76:79], v[56:59], v[140:143], v[76:79]
	v_fma_f32 v243, |v221|, s80, 1.0
	v_mfma_f32_16x16x32_f16 v[72:75], v[64:67], v[140:143], v[72:75]
	v_mul_f32_e32 v246, v220, v220
	v_mfma_f32_16x16x32_f16 v[28:31], v[56:59], v[148:151], v[28:31]
	v_rcp_f32_e32 v242, v242
	v_mfma_f32_16x16x32_f16 v[24:27], v[64:67], v[148:151], v[24:27]
	v_rcp_f32_e32 v243, v243
	v_mfma_f32_16x16x32_f16 v[12:15], v[56:59], v[156:159], v[12:15]
	v_mul_f32_e32 v247, v221, v221
	v_mul_f32_e32 v246, s90, v246
	v_mfma_f32_16x16x32_f16 v[8:11], v[64:67], v[156:159], v[8:11]
	v_mul_f32_e32 v247, s90, v247
	s_setprio 0
	s_barrier
	s_add_i32 s48, 0, 0x14000
	s_add_u32 s46, s46, s10
	s_addc_u32 s47, s47, s11
	s_mov_b32 m0, s61
	v_add_u32_e32 v64, s48, v128
	v_lshl_add_u64 v[166:167], s[46:47], 0, v[102:103]
	ds_read_b128 v[44:47], v64
	ds_read_b128 v[56:59], v64 offset:1024
	ds_read_b128 v[60:63], v64 offset:2048
	ds_read_b128 v[64:67], v64 offset:3072
	global_load_lds_dwordx4 v[166:167], off
	v_lshl_add_u64 v[168:169], s[46:47], 0, v[106:107]
	s_mov_b32 m0, s62
	s_nop 0
	global_load_lds_dwordx4 v[168:169], off
	s_waitcnt vmcnt(6)
	s_barrier
	s_waitcnt lgkmcnt(0)
	s_setprio 1
	s_waitcnt lgkmcnt(0)
	v_mfma_f32_16x16x32_f16 v[84:87], v[44:47], v[80:83], v[84:87]
	v_fma_f32 v244, v242, s82, v248
	v_mfma_f32_16x16x32_f16 v[52:55], v[44:47], v[136:139], v[52:55]
	v_fma_f32 v245, v243, s82, v248
	v_mfma_f32_16x16x32_f16 v[48:51], v[60:63], v[136:139], v[48:51]
	v_exp_f32_e32 v246, v246
	v_mfma_f32_16x16x32_f16 v[20:23], v[44:47], v[144:147], v[20:23]
	v_exp_f32_e32 v247, v247
	v_mfma_f32_16x16x32_f16 v[16:19], v[60:63], v[144:147], v[16:19]
	v_fmaak_f32 v244, v242, v244, 0x3f35f0e3
	v_fmaak_f32 v245, v243, v245, 0x3f35f0e3
	v_mfma_f32_16x16x32_f16 v[4:7], v[44:47], v[152:155], v[4:7]
	v_fmaak_f32 v244, v242, v244, 0xbe11a98e
	v_mfma_f32_16x16x32_f16 v[0:3], v[60:63], v[152:155], v[0:3]
	v_fmaak_f32 v245, v243, v245, 0xbe11a98e
	v_mfma_f32_16x16x32_f16 v[84:87], v[56:59], v[96:99], v[84:87]
	v_fmaak_f32 v244, v242, v244, 0x3e027906
	v_mfma_f32_16x16x32_f16 v[68:71], v[60:63], v[80:83], v[68:71]
	v_fmaak_f32 v245, v243, v245, 0x3e027906
	v_mfma_f32_16x16x32_f16 v[52:55], v[56:59], v[140:143], v[52:55]
	v_mul_f32_e32 v244, v242, v244
	v_mfma_f32_16x16x32_f16 v[48:51], v[64:67], v[140:143], v[48:51]
	v_mul_f32_e32 v245, v243, v245
	v_max_f32_e32 v242, 0, v220
	v_mfma_f32_16x16x32_f16 v[20:23], v[56:59], v[148:151], v[20:23]
	v_max_f32_e32 v243, 0, v221
	v_mfma_f32_16x16x32_f16 v[16:19], v[64:67], v[148:151], v[16:19]
	v_mul_f32_e32 v244, v244, v246
	v_mfma_f32_16x16x32_f16 v[4:7], v[56:59], v[156:159], v[4:7]
	v_mul_f32_e32 v245, v245, v247
	v_mfma_f32_16x16x32_f16 v[0:3], v[64:67], v[156:159], v[0:3]
	v_fma_f32 v244, -|v220|, v244, v242
	v_mfma_f32_16x16x32_f16 v[68:71], v[64:67], v[96:99], v[68:71]
	v_fma_f32 v245, -|v221|, v245, v243
	s_setprio 0
	s_barrier
	s_mov_b32 m0, s64
	v_lshl_add_u64 v[126:127], v[126:127], 0, s[22:23]
	ds_read_b128 v[44:47], v132
	ds_read_b128 v[56:59], v132 offset:1024
	ds_read_b128 v[60:63], v132 offset:2048
	ds_read_b128 v[64:67], v132 offset:3072
	ds_read_b128 v[80:83], v133
	ds_read_b128 v[96:99], v133 offset:1024
	ds_read_b128 v[136:139], v133 offset:2048
	ds_read_b128 v[140:143], v133 offset:3072
	ds_read_b128 v[144:147], v133 offset:4096
	ds_read_b128 v[148:151], v133 offset:5120
	ds_read_b128 v[152:155], v133 offset:6144
	ds_read_b128 v[156:159], v133 offset:7168
	global_load_lds_dwordx4 v[126:127], off
	v_lshl_add_u64 v[126:127], v[160:161], 0, s[22:23]
	s_mov_b32 m0, s65
	s_add_i32 s46, s76, s54
	global_load_lds_dwordx4 v[126:127], off
	v_lshl_add_u64 v[126:127], v[162:163], 0, s[22:23]
	s_mov_b32 m0, s46
	s_nop 0
	global_load_lds_dwordx4 v[126:127], off
	v_lshl_add_u64 v[126:127], v[164:165], 0, s[22:23]
	s_add_i32 m0, s46, 0x2000
	s_nop 0
	global_load_lds_dwordx4 v[126:127], off
	s_barrier
	s_waitcnt lgkmcnt(0)
	s_setprio 1
	s_waitcnt lgkmcnt(0)
	v_mfma_f32_16x16x32_f16 v[92:95], v[44:47], v[80:83], v[92:95]
	v_cvt_pk_f16_f32 v218, v244, v245
	v_fma_f32 v242, |v222|, s80, 1.0
	v_mfma_f32_16x16x32_f16 v[88:91], v[60:63], v[80:83], v[88:91]
	v_fma_f32 v243, |v223|, s80, 1.0
	v_mfma_f32_16x16x32_f16 v[76:79], v[44:47], v[136:139], v[76:79]
	v_mul_f32_e32 v246, v222, v222
	v_mfma_f32_16x16x32_f16 v[72:75], v[60:63], v[136:139], v[72:75]
	v_rcp_f32_e32 v242, v242
	v_mfma_f32_16x16x32_f16 v[28:31], v[44:47], v[144:147], v[28:31]
	v_rcp_f32_e32 v243, v243
	v_mfma_f32_16x16x32_f16 v[24:27], v[60:63], v[144:147], v[24:27]
	v_mul_f32_e32 v247, v223, v223
	v_mfma_f32_16x16x32_f16 v[12:15], v[44:47], v[152:155], v[12:15]
	v_mul_f32_e32 v246, s90, v246
	v_mul_f32_e32 v247, s90, v247
	v_mfma_f32_16x16x32_f16 v[8:11], v[60:63], v[152:155], v[8:11]
	v_fma_f32 v244, v242, s82, v248
	v_mfma_f32_16x16x32_f16 v[92:95], v[56:59], v[96:99], v[92:95]
	v_fma_f32 v245, v243, s82, v248
	v_mfma_f32_16x16x32_f16 v[88:91], v[64:67], v[96:99], v[88:91]
	v_exp_f32_e32 v246, v246
	v_mfma_f32_16x16x32_f16 v[76:79], v[56:59], v[140:143], v[76:79]
	v_exp_f32_e32 v247, v247
	v_mfma_f32_16x16x32_f16 v[72:75], v[64:67], v[140:143], v[72:75]
	v_fmaak_f32 v244, v242, v244, 0x3f35f0e3
	v_mfma_f32_16x16x32_f16 v[28:31], v[56:59], v[148:151], v[28:31]
	v_fmaak_f32 v245, v243, v245, 0x3f35f0e3
	v_fmaak_f32 v244, v242, v244, 0xbe11a98e
	v_mfma_f32_16x16x32_f16 v[24:27], v[64:67], v[148:151], v[24:27]
	v_fmaak_f32 v245, v243, v245, 0xbe11a98e
	v_mfma_f32_16x16x32_f16 v[12:15], v[56:59], v[156:159], v[12:15]
	v_fmaak_f32 v244, v242, v244, 0x3e027906
	v_mfma_f32_16x16x32_f16 v[8:11], v[64:67], v[156:159], v[8:11]
	v_fmaak_f32 v245, v243, v245, 0x3e027906
	s_setprio 0
	s_barrier
	s_add_i32 s46, s48, s54
	v_lshl_add_u64 v[126:127], v[166:167], 0, s[22:23]
	s_mov_b32 m0, s46
	ds_read_b128 v[44:47], v134
	ds_read_b128 v[56:59], v134 offset:1024
	ds_read_b128 v[60:63], v134 offset:2048
	ds_read_b128 v[64:67], v134 offset:3072
	global_load_lds_dwordx4 v[126:127], off
	v_lshl_add_u64 v[126:127], v[168:169], 0, s[22:23]
	s_add_i32 m0, s46, 0x2000
	s_nop 0
	global_load_lds_dwordx4 v[126:127], off
	s_waitcnt vmcnt(6)
	s_barrier
	s_waitcnt lgkmcnt(0)
	s_setprio 1
	s_waitcnt lgkmcnt(0)
	v_mfma_f32_16x16x32_f16 v[84:87], v[44:47], v[80:83], v[84:87]
	v_mul_f32_e32 v244, v242, v244
	v_mfma_f32_16x16x32_f16 v[68:71], v[60:63], v[80:83], v[68:71]
	v_mul_f32_e32 v245, v243, v245
	v_mfma_f32_16x16x32_f16 v[52:55], v[44:47], v[136:139], v[52:55]
	v_max_f32_e32 v242, 0, v222
	v_max_f32_e32 v243, 0, v223
	v_mfma_f32_16x16x32_f16 v[48:51], v[60:63], v[136:139], v[48:51]
	v_mul_f32_e32 v244, v244, v246
	v_mfma_f32_16x16x32_f16 v[20:23], v[44:47], v[144:147], v[20:23]
	v_mul_f32_e32 v245, v245, v247
	v_mfma_f32_16x16x32_f16 v[16:19], v[60:63], v[144:147], v[16:19]
	v_fma_f32 v244, -|v222|, v244, v242
	v_mfma_f32_16x16x32_f16 v[4:7], v[44:47], v[152:155], v[4:7]
	v_fma_f32 v245, -|v223|, v245, v243
	v_mfma_f32_16x16x32_f16 v[0:3], v[60:63], v[152:155], v[0:3]
	v_cvt_pk_f16_f32 v219, v244, v245
	v_mfma_f32_16x16x32_f16 v[84:87], v[56:59], v[96:99], v[84:87]
	v_lshl_add_u64 v[252:253], v[250:251], 0, s[94:95]
	global_store_dwordx4 v[252:253], v[216:219], off offset:256 sc1
	v_mfma_f32_16x16x32_f16 v[80:83], v[64:67], v[96:99], v[68:71]
	v_fma_f32 v242, |v232|, s80, 1.0
	v_mfma_f32_16x16x32_f16 v[52:55], v[56:59], v[140:143], v[52:55]
	v_fma_f32 v243, |v233|, s80, 1.0
	v_mfma_f32_16x16x32_f16 v[48:51], v[64:67], v[140:143], v[48:51]
	v_mul_f32_e32 v246, v232, v232
	v_mfma_f32_16x16x32_f16 v[20:23], v[56:59], v[148:151], v[20:23]
	v_rcp_f32_e32 v242, v242
	v_mfma_f32_16x16x32_f16 v[16:19], v[64:67], v[148:151], v[16:19]
	v_rcp_f32_e32 v243, v243
	v_mfma_f32_16x16x32_f16 v[4:7], v[56:59], v[156:159], v[4:7]
	v_mul_f32_e32 v247, v233, v233
	v_mul_f32_e32 v246, s90, v246
	v_mfma_f32_16x16x32_f16 v[0:3], v[64:67], v[156:159], v[0:3]
	v_mul_f32_e32 v247, s90, v247
	s_setprio 0
	s_barrier
	s_add_i32 s75, s75, 3
	s_add_u32 s44, s44, 0x180
	s_addc_u32 s45, s45, 0
	s_add_u32 s46, s40, s44
	s_addc_u32 s47, s41, s45
	s_add_u32 s46, s46, 0x180
	s_addc_u32 s47, s47, 0
	s_add_u32 s48, s42, s44
	s_addc_u32 s49, s43, s45
	s_add_u32 s76, s48, 0x180
	s_addc_u32 s77, s49, 0
	s_cmp_eq_u32 s67, s75
	s_cselect_b32 s49, s7, s47
	s_cselect_b32 s48, s6, s46
	s_cselect_b32 s47, s5, s77
	s_cselect_b32 s46, s4, s76
	s_add_i32 s76, s19, s54
	v_lshl_add_u64 v[126:127], v[32:33], 0, s[44:45]
	s_mov_b32 m0, s76
	ds_read_b128 v[44:47], v130 offset:16384
	ds_read_b128 v[56:59], v130 offset:17408
	ds_read_b128 v[60:63], v130 offset:18432
	ds_read_b128 v[64:67], v130 offset:19456
	ds_read_b128 v[68:71], v131
	ds_read_b128 v[96:99], v131 offset:1024
	ds_read_b128 v[136:139], v131 offset:2048
	ds_read_b128 v[140:143], v131 offset:3072
	ds_read_b128 v[144:147], v131 offset:4096
	ds_read_b128 v[148:151], v131 offset:5120
	ds_read_b128 v[152:155], v131 offset:6144
	ds_read_b128 v[156:159], v131 offset:7168
	global_load_lds_dwordx4 v[126:127], off
	v_lshl_add_u64 v[126:127], v[34:35], 0, s[44:45]
	s_add_i32 m0, s76, 0x2000
	s_add_i32 s76, s27, s54
	global_load_lds_dwordx4 v[126:127], off
	v_lshl_add_u64 v[126:127], v[36:37], 0, s[44:45]
	s_mov_b32 m0, s76
	s_nop 0
	global_load_lds_dwordx4 v[126:127], off
	v_lshl_add_u64 v[126:127], v[38:39], 0, s[44:45]
	s_add_i32 m0, s76, 0x2000
	s_nop 0
	global_load_lds_dwordx4 v[126:127], off
	s_barrier
	s_waitcnt lgkmcnt(0)
	s_setprio 1
	s_waitcnt lgkmcnt(0)
	v_mfma_f32_16x16x32_f16 v[92:95], v[44:47], v[68:71], v[92:95]
	v_fma_f32 v244, v242, s82, v248
	v_mfma_f32_16x16x32_f16 v[88:91], v[60:63], v[68:71], v[88:91]
	v_fma_f32 v245, v243, s82, v248
	v_mfma_f32_16x16x32_f16 v[76:79], v[44:47], v[136:139], v[76:79]
	v_exp_f32_e32 v246, v246
	v_mfma_f32_16x16x32_f16 v[72:75], v[60:63], v[136:139], v[72:75]
	v_exp_f32_e32 v247, v247
	v_mfma_f32_16x16x32_f16 v[28:31], v[44:47], v[144:147], v[28:31]
	v_fmaak_f32 v244, v242, v244, 0x3f35f0e3
	v_fmaak_f32 v245, v243, v245, 0x3f35f0e3
	v_mfma_f32_16x16x32_f16 v[24:27], v[60:63], v[144:147], v[24:27]
	v_fmaak_f32 v244, v242, v244, 0xbe11a98e
	v_mfma_f32_16x16x32_f16 v[12:15], v[44:47], v[152:155], v[12:15]
	v_fmaak_f32 v245, v243, v245, 0xbe11a98e
	v_mfma_f32_16x16x32_f16 v[8:11], v[60:63], v[152:155], v[8:11]
	v_fmaak_f32 v244, v242, v244, 0x3e027906
	v_mfma_f32_16x16x32_f16 v[92:95], v[56:59], v[96:99], v[92:95]
	v_fmaak_f32 v245, v243, v245, 0x3e027906
	v_mfma_f32_16x16x32_f16 v[88:91], v[64:67], v[96:99], v[88:91]
	v_mul_f32_e32 v244, v242, v244
	v_mfma_f32_16x16x32_f16 v[76:79], v[56:59], v[140:143], v[76:79]
	v_mul_f32_e32 v245, v243, v245
	v_max_f32_e32 v242, 0, v232
	v_mfma_f32_16x16x32_f16 v[72:75], v[64:67], v[140:143], v[72:75]
	v_max_f32_e32 v243, 0, v233
	v_mfma_f32_16x16x32_f16 v[28:31], v[56:59], v[148:151], v[28:31]
	v_mul_f32_e32 v244, v244, v246
	v_mfma_f32_16x16x32_f16 v[24:27], v[64:67], v[148:151], v[24:27]
	v_mul_f32_e32 v245, v245, v247
	v_mfma_f32_16x16x32_f16 v[12:15], v[56:59], v[156:159], v[12:15]
	v_fma_f32 v244, -|v232|, v244, v242
	v_mfma_f32_16x16x32_f16 v[8:11], v[64:67], v[156:159], v[8:11]
	v_fma_f32 v245, -|v233|, v245, v243
	s_setprio 0
	s_barrier
	s_add_i32 s76, s68, s54
	v_lshl_add_u64 v[126:127], v[40:41], 0, s[44:45]
	s_mov_b32 m0, s76
	ds_read_b128 v[44:47], v130 offset:32768
	ds_read_b128 v[56:59], v130 offset:33792
	ds_read_b128 v[60:63], v130 offset:34816
	ds_read_b128 v[64:67], v130 offset:35840
	global_load_lds_dwordx4 v[126:127], off
	v_lshl_add_u64 v[126:127], v[42:43], 0, s[44:45]
	s_add_i32 m0, s76, 0x2000
	s_nop 0
	global_load_lds_dwordx4 v[126:127], off
	s_waitcnt vmcnt(7)
	s_barrier
	s_waitcnt lgkmcnt(0)
	s_setprio 1
	s_waitcnt lgkmcnt(0)
	v_mfma_f32_16x16x32_f16 v[84:87], v[44:47], v[68:71], v[84:87]
	v_cvt_pk_f16_f32 v232, v244, v245
	v_fma_f32 v242, |v234|, s80, 1.0
	v_mfma_f32_16x16x32_f16 v[52:55], v[44:47], v[136:139], v[52:55]
	v_fma_f32 v243, |v235|, s80, 1.0
	v_mfma_f32_16x16x32_f16 v[48:51], v[60:63], v[136:139], v[48:51]
	v_mul_f32_e32 v246, v234, v234
	v_mfma_f32_16x16x32_f16 v[20:23], v[44:47], v[144:147], v[20:23]
	v_rcp_f32_e32 v242, v242
	v_mfma_f32_16x16x32_f16 v[16:19], v[60:63], v[144:147], v[16:19]
	v_rcp_f32_e32 v243, v243
	v_mfma_f32_16x16x32_f16 v[4:7], v[44:47], v[152:155], v[4:7]
	v_mul_f32_e32 v247, v235, v235
	v_mfma_f32_16x16x32_f16 v[0:3], v[60:63], v[152:155], v[0:3]
	v_mul_f32_e32 v246, s90, v246
	v_mul_f32_e32 v247, s90, v247
	v_mfma_f32_16x16x32_f16 v[84:87], v[56:59], v[96:99], v[84:87]
	v_fma_f32 v244, v242, s82, v248
	v_mfma_f32_16x16x32_f16 v[68:71], v[60:63], v[68:71], v[80:83]
	v_fma_f32 v245, v243, s82, v248
	v_mfma_f32_16x16x32_f16 v[52:55], v[56:59], v[140:143], v[52:55]
	v_exp_f32_e32 v246, v246
	v_mfma_f32_16x16x32_f16 v[48:51], v[64:67], v[140:143], v[48:51]
	v_exp_f32_e32 v247, v247
	v_mfma_f32_16x16x32_f16 v[20:23], v[56:59], v[148:151], v[20:23]
	v_fmaak_f32 v244, v242, v244, 0x3f35f0e3
	v_mfma_f32_16x16x32_f16 v[16:19], v[64:67], v[148:151], v[16:19]
	v_fmaak_f32 v245, v243, v245, 0x3f35f0e3
	v_fmaak_f32 v244, v242, v244, 0xbe11a98e
	v_mfma_f32_16x16x32_f16 v[4:7], v[56:59], v[156:159], v[4:7]
	v_fmaak_f32 v245, v243, v245, 0xbe11a98e
	v_mfma_f32_16x16x32_f16 v[0:3], v[64:67], v[156:159], v[0:3]
	v_fmaak_f32 v244, v242, v244, 0x3e027906
	v_mfma_f32_16x16x32_f16 v[68:71], v[64:67], v[96:99], v[68:71]
	v_fmaak_f32 v245, v243, v245, 0x3e027906
	s_setprio 0
	s_barrier
	s_add_i32 s76, 0, 0x10000
	s_mov_b32 m0, s57
	v_add_u32_e32 v64, s76, v128
	v_lshl_add_u64 v[126:127], s[48:49], 0, v[100:101]
	ds_read_b128 v[44:47], v64
	ds_read_b128 v[56:59], v64 offset:1024
	ds_read_b128 v[60:63], v64 offset:2048
	ds_read_b128 v[64:67], v64 offset:3072
	ds_read_b128 v[80:83], v131 offset:49152
	ds_read_b128 v[96:99], v131 offset:50176
	ds_read_b128 v[136:139], v131 offset:51200
	ds_read_b128 v[140:143], v131 offset:52224
	ds_read_b128 v[144:147], v131 offset:53248
	ds_read_b128 v[148:151], v131 offset:54272
	ds_read_b128 v[152:155], v131 offset:55296
	ds_read_b128 v[156:159], v131 offset:56320
	global_load_lds_dwordx4 v[126:127], off
	v_lshl_add_u64 v[160:161], s[48:49], 0, v[104:105]
	s_mov_b32 m0, s58
	v_lshl_add_u64 v[162:163], s[46:47], 0, v[102:103]
	global_load_lds_dwordx4 v[160:161], off
	s_mov_b32 m0, s59
	v_lshl_add_u64 v[164:165], s[46:47], 0, v[106:107]
	global_load_lds_dwordx4 v[162:163], off
	s_mov_b32 m0, s60
	s_nop 0
	global_load_lds_dwordx4 v[164:165], off
	s_barrier
	s_waitcnt lgkmcnt(0)
	s_setprio 1
	s_waitcnt lgkmcnt(0)
	v_mfma_f32_16x16x32_f16 v[92:95], v[44:47], v[80:83], v[92:95]
	v_mul_f32_e32 v244, v242, v244
	v_mfma_f32_16x16x32_f16 v[88:91], v[60:63], v[80:83], v[88:91]
	v_mul_f32_e32 v245, v243, v245
	v_mfma_f32_16x16x32_f16 v[76:79], v[44:47], v[136:139], v[76:79]
	v_max_f32_e32 v242, 0, v234
	v_max_f32_e32 v243, 0, v235
	v_mfma_f32_16x16x32_f16 v[72:75], v[60:63], v[136:139], v[72:75]
	v_mul_f32_e32 v244, v244, v246
	v_mfma_f32_16x16x32_f16 v[28:31], v[44:47], v[144:147], v[28:31]
	v_mul_f32_e32 v245, v245, v247
	v_mfma_f32_16x16x32_f16 v[24:27], v[60:63], v[144:147], v[24:27]
	v_fma_f32 v244, -|v234|, v244, v242
	v_mfma_f32_16x16x32_f16 v[12:15], v[44:47], v[152:155], v[12:15]
	v_fma_f32 v245, -|v235|, v245, v243
	v_mfma_f32_16x16x32_f16 v[8:11], v[60:63], v[152:155], v[8:11]
	v_cvt_pk_f16_f32 v233, v244, v245
	v_mfma_f32_16x16x32_f16 v[92:95], v[56:59], v[96:99], v[92:95]
	v_fma_f32 v242, |v236|, s80, 1.0
	v_fma_f32 v243, |v237|, s80, 1.0
	v_mfma_f32_16x16x32_f16 v[88:91], v[64:67], v[96:99], v[88:91]
	v_mul_f32_e32 v246, v236, v236
	v_mfma_f32_16x16x32_f16 v[76:79], v[56:59], v[140:143], v[76:79]
	v_rcp_f32_e32 v242, v242
	v_mfma_f32_16x16x32_f16 v[72:75], v[64:67], v[140:143], v[72:75]
	v_rcp_f32_e32 v243, v243
	v_mfma_f32_16x16x32_f16 v[28:31], v[56:59], v[148:151], v[28:31]
	v_mul_f32_e32 v247, v237, v237
	v_mfma_f32_16x16x32_f16 v[24:27], v[64:67], v[148:151], v[24:27]
	v_mul_f32_e32 v246, s90, v246
	v_mfma_f32_16x16x32_f16 v[12:15], v[56:59], v[156:159], v[12:15]
	v_mul_f32_e32 v247, s90, v247
	v_fma_f32 v244, v242, s82, v248
	v_mfma_f32_16x16x32_f16 v[8:11], v[64:67], v[156:159], v[8:11]
	v_fma_f32 v245, v243, s82, v248
	s_setprio 0
	s_barrier
	s_add_i32 s48, 0, 0x14000
	s_add_u32 s46, s46, s10
	s_addc_u32 s47, s47, s11
	s_mov_b32 m0, s61
	v_add_u32_e32 v64, s48, v128
	v_lshl_add_u64 v[166:167], s[46:47], 0, v[102:103]
	ds_read_b128 v[44:47], v64
	ds_read_b128 v[56:59], v64 offset:1024
	ds_read_b128 v[60:63], v64 offset:2048
	ds_read_b128 v[64:67], v64 offset:3072
	global_load_lds_dwordx4 v[166:167], off
	v_lshl_add_u64 v[168:169], s[46:47], 0, v[106:107]
	s_mov_b32 m0, s62
	s_nop 0
	global_load_lds_dwordx4 v[168:169], off
	s_waitcnt vmcnt(6)
	s_barrier
	s_waitcnt lgkmcnt(0)
	s_setprio 1
	s_waitcnt lgkmcnt(0)
	v_mfma_f32_16x16x32_f16 v[84:87], v[44:47], v[80:83], v[84:87]
	v_exp_f32_e32 v246, v246
	v_mfma_f32_16x16x32_f16 v[52:55], v[44:47], v[136:139], v[52:55]
	v_exp_f32_e32 v247, v247
	v_mfma_f32_16x16x32_f16 v[48:51], v[60:63], v[136:139], v[48:51]
	v_fmaak_f32 v244, v242, v244, 0x3f35f0e3
	v_mfma_f32_16x16x32_f16 v[20:23], v[44:47], v[144:147], v[20:23]
	v_fmaak_f32 v245, v243, v245, 0x3f35f0e3
	v_mfma_f32_16x16x32_f16 v[16:19], v[60:63], v[144:147], v[16:19]
	v_fmaak_f32 v244, v242, v244, 0xbe11a98e
	v_fmaak_f32 v245, v243, v245, 0xbe11a98e
	v_mfma_f32_16x16x32_f16 v[4:7], v[44:47], v[152:155], v[4:7]
	v_fmaak_f32 v244, v242, v244, 0x3e027906
	v_mfma_f32_16x16x32_f16 v[0:3], v[60:63], v[152:155], v[0:3]
	v_fmaak_f32 v245, v243, v245, 0x3e027906
	v_mfma_f32_16x16x32_f16 v[84:87], v[56:59], v[96:99], v[84:87]
	v_mul_f32_e32 v244, v242, v244
	v_mfma_f32_16x16x32_f16 v[68:71], v[60:63], v[80:83], v[68:71]
	v_mul_f32_e32 v245, v243, v245
	v_mfma_f32_16x16x32_f16 v[52:55], v[56:59], v[140:143], v[52:55]
	v_max_f32_e32 v242, 0, v236
	v_mfma_f32_16x16x32_f16 v[48:51], v[64:67], v[140:143], v[48:51]
	v_max_f32_e32 v243, 0, v237
	v_mul_f32_e32 v244, v244, v246
	v_mfma_f32_16x16x32_f16 v[20:23], v[56:59], v[148:151], v[20:23]
	v_mul_f32_e32 v245, v245, v247
	v_mfma_f32_16x16x32_f16 v[16:19], v[64:67], v[148:151], v[16:19]
	v_fma_f32 v244, -|v236|, v244, v242
	v_mfma_f32_16x16x32_f16 v[4:7], v[56:59], v[156:159], v[4:7]
	v_fma_f32 v245, -|v237|, v245, v243
	v_mfma_f32_16x16x32_f16 v[0:3], v[64:67], v[156:159], v[0:3]
	v_cvt_pk_f16_f32 v234, v244, v245
	v_mfma_f32_16x16x32_f16 v[68:71], v[64:67], v[96:99], v[68:71]
	v_fma_f32 v242, |v238|, s80, 1.0
	s_setprio 0
	s_barrier
	s_mov_b32 m0, s64
	v_lshl_add_u64 v[126:127], v[126:127], 0, s[22:23]
	ds_read_b128 v[44:47], v132
	ds_read_b128 v[56:59], v132 offset:1024
	ds_read_b128 v[60:63], v132 offset:2048
	ds_read_b128 v[64:67], v132 offset:3072
	ds_read_b128 v[80:83], v133
	ds_read_b128 v[96:99], v133 offset:1024
	ds_read_b128 v[136:139], v133 offset:2048
	ds_read_b128 v[140:143], v133 offset:3072
	ds_read_b128 v[144:147], v133 offset:4096
	ds_read_b128 v[148:151], v133 offset:5120
	ds_read_b128 v[152:155], v133 offset:6144
	ds_read_b128 v[156:159], v133 offset:7168
	global_load_lds_dwordx4 v[126:127], off
	v_lshl_add_u64 v[126:127], v[160:161], 0, s[22:23]
	s_mov_b32 m0, s65
	s_add_i32 s46, s76, s54
	global_load_lds_dwordx4 v[126:127], off
	v_lshl_add_u64 v[126:127], v[162:163], 0, s[22:23]
	s_mov_b32 m0, s46
	s_nop 0
	global_load_lds_dwordx4 v[126:127], off
	v_lshl_add_u64 v[126:127], v[164:165], 0, s[22:23]
	s_add_i32 m0, s46, 0x2000
	s_nop 0
	global_load_lds_dwordx4 v[126:127], off
	s_barrier
	s_waitcnt lgkmcnt(0)
	s_setprio 1
	s_waitcnt lgkmcnt(0)
	v_mfma_f32_16x16x32_f16 v[92:95], v[44:47], v[80:83], v[92:95]
	v_fma_f32 v243, |v239|, s80, 1.0
	v_mul_f32_e32 v246, v238, v238
	v_mfma_f32_16x16x32_f16 v[88:91], v[60:63], v[80:83], v[88:91]
	v_rcp_f32_e32 v242, v242
	v_mfma_f32_16x16x32_f16 v[76:79], v[44:47], v[136:139], v[76:79]
	v_rcp_f32_e32 v243, v243
	v_mfma_f32_16x16x32_f16 v[72:75], v[60:63], v[136:139], v[72:75]
	v_mul_f32_e32 v247, v239, v239
	v_mfma_f32_16x16x32_f16 v[28:31], v[44:47], v[144:147], v[28:31]
	v_mul_f32_e32 v246, s90, v246
	v_mfma_f32_16x16x32_f16 v[24:27], v[60:63], v[144:147], v[24:27]
	v_mul_f32_e32 v247, s90, v247
	v_mfma_f32_16x16x32_f16 v[12:15], v[44:47], v[152:155], v[12:15]
	v_fma_f32 v244, v242, s82, v248
	v_fma_f32 v245, v243, s82, v248
	v_mfma_f32_16x16x32_f16 v[8:11], v[60:63], v[152:155], v[8:11]
	v_exp_f32_e32 v246, v246
	v_mfma_f32_16x16x32_f16 v[92:95], v[56:59], v[96:99], v[92:95]
	v_exp_f32_e32 v247, v247
	v_mfma_f32_16x16x32_f16 v[88:91], v[64:67], v[96:99], v[88:91]
	v_fmaak_f32 v244, v242, v244, 0x3f35f0e3
	v_mfma_f32_16x16x32_f16 v[76:79], v[56:59], v[140:143], v[76:79]
	v_fmaak_f32 v245, v243, v245, 0x3f35f0e3
	v_mfma_f32_16x16x32_f16 v[72:75], v[64:67], v[140:143], v[72:75]
	v_fmaak_f32 v244, v242, v244, 0xbe11a98e
	v_mfma_f32_16x16x32_f16 v[28:31], v[56:59], v[148:151], v[28:31]
	v_fmaak_f32 v245, v243, v245, 0xbe11a98e
	v_fmaak_f32 v244, v242, v244, 0x3e027906
	v_mfma_f32_16x16x32_f16 v[24:27], v[64:67], v[148:151], v[24:27]
	v_fmaak_f32 v245, v243, v245, 0x3e027906
	v_mfma_f32_16x16x32_f16 v[12:15], v[56:59], v[156:159], v[12:15]
	v_mul_f32_e32 v244, v242, v244
	v_mfma_f32_16x16x32_f16 v[8:11], v[64:67], v[156:159], v[8:11]
	v_mul_f32_e32 v245, v243, v245
	s_setprio 0
	s_barrier
	s_add_i32 s46, s48, s54
	v_lshl_add_u64 v[126:127], v[166:167], 0, s[22:23]
	s_mov_b32 m0, s46
	ds_read_b128 v[44:47], v134
	ds_read_b128 v[56:59], v134 offset:1024
	ds_read_b128 v[60:63], v134 offset:2048
	ds_read_b128 v[64:67], v134 offset:3072
	global_load_lds_dwordx4 v[126:127], off
	v_lshl_add_u64 v[126:127], v[168:169], 0, s[22:23]
	s_add_i32 m0, s46, 0x2000
	s_nop 0
	global_load_lds_dwordx4 v[126:127], off
	s_waitcnt vmcnt(6)
	s_barrier
	s_waitcnt lgkmcnt(0)
	s_setprio 1
	s_waitcnt lgkmcnt(0)
	v_mfma_f32_16x16x32_f16 v[84:87], v[44:47], v[80:83], v[84:87]
	v_max_f32_e32 v242, 0, v238
	v_mfma_f32_16x16x32_f16 v[68:71], v[60:63], v[80:83], v[68:71]
	v_max_f32_e32 v243, 0, v239
	v_mfma_f32_16x16x32_f16 v[52:55], v[44:47], v[136:139], v[52:55]
	v_mul_f32_e32 v244, v244, v246
	v_mul_f32_e32 v245, v245, v247
	v_mfma_f32_16x16x32_f16 v[48:51], v[60:63], v[136:139], v[48:51]
	v_fma_f32 v244, -|v238|, v244, v242
	v_mfma_f32_16x16x32_f16 v[20:23], v[44:47], v[144:147], v[20:23]
	v_fma_f32 v245, -|v239|, v245, v243
	v_mfma_f32_16x16x32_f16 v[16:19], v[60:63], v[144:147], v[16:19]
	v_cvt_pk_f16_f32 v235, v244, v245
	v_mfma_f32_16x16x32_f16 v[4:7], v[44:47], v[152:155], v[4:7]
	v_lshl_add_u64 v[252:253], v[250:251], 0, s[96:97]
	v_mfma_f32_16x16x32_f16 v[0:3], v[60:63], v[152:155], v[0:3]
	global_store_dwordx4 v[252:253], v[232:235], off offset:256 sc1
	v_mfma_f32_16x16x32_f16 v[84:87], v[56:59], v[96:99], v[84:87]
	v_mfma_f32_16x16x32_f16 v[80:83], v[64:67], v[96:99], v[68:71]
	v_mfma_f32_16x16x32_f16 v[52:55], v[56:59], v[140:143], v[52:55]
	v_mfma_f32_16x16x32_f16 v[48:51], v[64:67], v[140:143], v[48:51]
	v_mfma_f32_16x16x32_f16 v[20:23], v[56:59], v[148:151], v[20:23]
	v_mfma_f32_16x16x32_f16 v[16:19], v[64:67], v[148:151], v[16:19]
	v_mfma_f32_16x16x32_f16 v[4:7], v[56:59], v[156:159], v[4:7]
	v_mfma_f32_16x16x32_f16 v[0:3], v[64:67], v[156:159], v[0:3]
	s_setprio 0
	s_barrier
	s_add_i32 s75, s75, 3
	s_add_u32 s44, s44, 0x180
	s_addc_u32 s45, s45, 0
	s_branch .LBB5_42
